# code placement: K-loop head labels aligned to 64 bytes (.p2align 6)
# speedup vs baseline: 1.0051x; 1.0015x over previous
.Lzs_0:
	v_mov_b64_e32 v[2:3], 0
	v_mov_b64_e32 v[4:5], 0
	v_mov_b64_e32 v[6:7], 0
	v_mov_b64_e32 v[8:9], 0
	v_mov_b64_e32 v[10:11], 0
	v_mov_b64_e32 v[12:13], 0
	v_mov_b64_e32 v[14:15], 0
	v_mov_b64_e32 v[16:17], 0
	v_mov_b64_e32 v[18:19], 0
	v_mov_b64_e32 v[20:21], 0
	v_mov_b64_e32 v[22:23], 0
	v_mov_b64_e32 v[24:25], 0
	v_mov_b64_e32 v[26:27], 0
	v_mov_b64_e32 v[28:29], 0
	v_mov_b64_e32 v[30:31], 0
	v_mov_b64_e32 v[32:33], 0
	v_mov_b64_e32 v[34:35], 0
	v_mov_b64_e32 v[36:37], 0
	v_mov_b64_e32 v[38:39], 0
	v_mov_b64_e32 v[40:41], 0
	v_mov_b64_e32 v[42:43], 0
	v_mov_b64_e32 v[44:45], 0
	v_mov_b64_e32 v[46:47], 0
	v_mov_b64_e32 v[48:49], 0
	v_mov_b64_e32 v[50:51], 0
	v_mov_b64_e32 v[52:53], 0
	v_mov_b64_e32 v[54:55], 0
	v_mov_b64_e32 v[56:57], 0
	v_mov_b64_e32 v[58:59], 0
	v_mov_b64_e32 v[60:61], 0
	v_mov_b64_e32 v[62:63], 0
	v_mov_b64_e32 v[64:65], 0
	v_mov_b64_e32 v[66:67], 0
	v_mov_b64_e32 v[68:69], 0
	v_mov_b64_e32 v[70:71], 0
	v_mov_b64_e32 v[72:73], 0
	v_mov_b64_e32 v[74:75], 0
	v_mov_b64_e32 v[76:77], 0
	v_mov_b64_e32 v[78:79], 0
	v_mov_b64_e32 v[80:81], 0
	v_mov_b64_e32 v[82:83], 0
	v_mov_b64_e32 v[84:85], 0
	v_mov_b64_e32 v[86:87], 0
	v_mov_b64_e32 v[88:89], 0
	v_mov_b64_e32 v[90:91], 0
	v_mov_b64_e32 v[92:93], 0
	v_mov_b64_e32 v[94:95], 0
	v_mov_b64_e32 v[96:97], 0
	v_mov_b64_e32 v[98:99], 0
	v_mov_b64_e32 v[100:101], 0
	v_mov_b64_e32 v[102:103], 0
	v_mov_b64_e32 v[104:105], 0
	v_mov_b64_e32 v[106:107], 0
	v_mov_b64_e32 v[108:109], 0
	v_mov_b64_e32 v[110:111], 0
	v_mov_b64_e32 v[112:113], 0
	v_mov_b64_e32 v[114:115], 0
	v_mov_b64_e32 v[116:117], 0
	v_mov_b64_e32 v[118:119], 0
	v_mov_b64_e32 v[120:121], 0
	v_mov_b64_e32 v[122:123], 0
	v_mov_b64_e32 v[124:125], 0
	v_mov_b64_e32 v[126:127], 0
	v_mov_b64_e32 v[128:129], 0
	s_branch .LBB0_297
	.p2align 6
.LBB0_290:
	s_mov_b64 s[2:3], 0
	.p2align 6

.LBB0_294:
	s_andn2_b64 vcc, exec, s[8:9]
	s_waitcnt lgkmcnt(0)
	s_cbranch_vccnz .Lzs_0
	s_add_i32 s14, s71, 0x80
	s_addk_i32 s70, 0x100
	s_mov_b32 s71, 0
	ds_read_b128 v[160:163], v144
	ds_read_b128 v[164:167], v145
	ds_read_b128 v[168:171], v140
	ds_read_b128 v[172:175], v141
	ds_read_b128 v[176:179], v146
	ds_read_b128 v[180:183], v147
	ds_read_b128 v[184:187], v148
	ds_read_b128 v[188:191], v149
	s_add_i32 s72, s14, 0x80
	s_cmp_eq_u32 s54, s71
	s_cselect_b32 s73, s13, s70
	s_cselect_b32 s72, s15, s72
	v_add_u32_e32 v159, s14, v157
	s_add_i32 m0, s22, 0xc000
	ds_read_b128 v[192:195], v158
	ds_read_b128 v[196:199], v158 offset:1024
	ds_read_b128 v[200:203], v158 offset:2048
	ds_read_b128 v[204:207], v158 offset:3072
	ds_read_b128 v[214:217], v158 offset:4096
	ds_read_b128 v[218:221], v158 offset:5120
	ds_read_b128 v[222:225], v158 offset:6144
	ds_read_b128 v[226:229], v158 offset:7168
	global_load_lds_dwordx4 v159, s[4:5]
	v_add_u32_e32 v159, s14, v156
	s_add_i32 m0, s22, 0xe000
	s_nop 0
	global_load_lds_dwordx4 v159, s[4:5]
	s_waitcnt vmcnt(8)
	s_waitcnt lgkmcnt(0)
	s_barrier
	s_setprio 1
	s_waitcnt lgkmcnt(0)
	v_mfma_f32_16x16x32_bf16 v[122:125], v[168:171], v[192:195], 0
	v_mfma_f32_16x16x32_bf16 v[126:129], v[164:167], v[192:195], 0
	v_mfma_f32_16x16x32_bf16 v[110:113], v[168:171], v[200:203], 0
	v_mfma_f32_16x16x32_bf16 v[106:109], v[164:167], v[200:203], 0
	v_mfma_f32_16x16x32_bf16 v[94:97], v[168:171], v[214:217], 0
	v_mfma_f32_16x16x32_bf16 v[90:93], v[164:167], v[214:217], 0
	v_mfma_f32_16x16x32_bf16 v[78:81], v[168:171], v[222:225], 0
	v_mfma_f32_16x16x32_bf16 v[74:77], v[164:167], v[222:225], 0
	v_mfma_f32_16x16x32_bf16 v[122:125], v[160:163], v[196:199], v[122:125]
	v_mfma_f32_16x16x32_bf16 v[126:129], v[176:179], v[196:199], v[126:129]
	v_mfma_f32_16x16x32_bf16 v[110:113], v[160:163], v[204:207], v[110:113]
	v_mfma_f32_16x16x32_bf16 v[106:109], v[176:179], v[204:207], v[106:109]
	v_mfma_f32_16x16x32_bf16 v[94:97], v[160:163], v[218:221], v[94:97]
	v_mfma_f32_16x16x32_bf16 v[90:93], v[176:179], v[218:221], v[90:93]
	v_mfma_f32_16x16x32_bf16 v[78:81], v[160:163], v[226:229], v[78:81]
	v_mfma_f32_16x16x32_bf16 v[74:77], v[176:179], v[226:229], v[74:77]
	s_setprio 0
	s_setprio 1
	v_mfma_f32_16x16x32_bf16 v[118:121], v[172:175], v[192:195], 0
	v_mfma_f32_16x16x32_bf16 v[114:117], v[184:187], v[192:195], 0
	v_mfma_f32_16x16x32_bf16 v[102:105], v[172:175], v[200:203], 0
	v_mfma_f32_16x16x32_bf16 v[98:101], v[184:187], v[200:203], 0
	v_mfma_f32_16x16x32_bf16 v[86:89], v[172:175], v[214:217], 0
	v_mfma_f32_16x16x32_bf16 v[82:85], v[184:187], v[214:217], 0
	v_mfma_f32_16x16x32_bf16 v[70:73], v[172:175], v[222:225], 0
	v_mfma_f32_16x16x32_bf16 v[66:69], v[184:187], v[222:225], 0
	v_mfma_f32_16x16x32_bf16 v[118:121], v[180:183], v[196:199], v[118:121]
	v_mfma_f32_16x16x32_bf16 v[114:117], v[188:191], v[196:199], v[114:117]
	v_mfma_f32_16x16x32_bf16 v[102:105], v[180:183], v[204:207], v[102:105]
	v_mfma_f32_16x16x32_bf16 v[98:101], v[188:191], v[204:207], v[98:101]
	v_mfma_f32_16x16x32_bf16 v[86:89], v[180:183], v[218:221], v[86:89]
	v_mfma_f32_16x16x32_bf16 v[82:85], v[188:191], v[218:221], v[82:85]
	v_mfma_f32_16x16x32_bf16 v[70:73], v[180:183], v[226:229], v[70:73]
	v_mfma_f32_16x16x32_bf16 v[66:69], v[188:191], v[226:229], v[66:69]
	s_setprio 0
	s_barrier
	s_mov_b32 m0, s23
	v_add_u32_e32 v159, s73, v134
	ds_read_b128 v[192:195], v158 offset:16384
	ds_read_b128 v[196:199], v158 offset:17408
	ds_read_b128 v[200:203], v158 offset:18432
	ds_read_b128 v[204:207], v158 offset:19456
	ds_read_b128 v[214:217], v158 offset:20480
	ds_read_b128 v[218:221], v158 offset:21504
	ds_read_b128 v[222:225], v158 offset:22528
	ds_read_b128 v[226:229], v158 offset:23552
	global_load_lds_dwordx4 v159, s[20:21]
	v_add_u32_e32 v159, s17, v159
	s_mov_b32 m0, s28
	s_nop 0
	global_load_lds_dwordx4 v159, s[20:21]
	v_add_u32_e32 v159, s73, v135
	s_mov_b32 m0, s29
	s_nop 0
	global_load_lds_dwordx4 v159, s[20:21]
	v_add_u32_e32 v159, s17, v159
	s_mov_b32 m0, s30
	s_nop 0
	global_load_lds_dwordx4 v159, s[20:21]
	v_add_u32_e32 v159, s72, v1
	s_mov_b32 m0, s22
	s_nop 0
	global_load_lds_dwordx4 v159, s[4:5]
	v_add_u32_e32 v159, s16, v159
	s_mov_b32 m0, s31
	s_nop 0
	global_load_lds_dwordx4 v159, s[4:5]
	s_waitcnt vmcnt(8)
	s_waitcnt lgkmcnt(0)
	s_barrier
	s_setprio 1
	s_waitcnt lgkmcnt(0)
	v_mfma_f32_16x16x32_bf16 v[62:65], v[168:171], v[192:195], 0
	v_mfma_f32_16x16x32_bf16 v[58:61], v[164:167], v[192:195], 0
	v_mfma_f32_16x16x32_bf16 v[46:49], v[168:171], v[200:203], 0
	v_mfma_f32_16x16x32_bf16 v[42:45], v[164:167], v[200:203], 0
	v_mfma_f32_16x16x32_bf16 v[30:33], v[168:171], v[214:217], 0
	v_mfma_f32_16x16x32_bf16 v[26:29], v[164:167], v[214:217], 0
	v_mfma_f32_16x16x32_bf16 v[14:17], v[168:171], v[222:225], 0
	v_mfma_f32_16x16x32_bf16 v[10:13], v[164:167], v[222:225], 0
	v_mfma_f32_16x16x32_bf16 v[62:65], v[160:163], v[196:199], v[62:65]
	v_mfma_f32_16x16x32_bf16 v[58:61], v[176:179], v[196:199], v[58:61]
	v_mfma_f32_16x16x32_bf16 v[46:49], v[160:163], v[204:207], v[46:49]
	v_mfma_f32_16x16x32_bf16 v[42:45], v[176:179], v[204:207], v[42:45]
	v_mfma_f32_16x16x32_bf16 v[30:33], v[160:163], v[218:221], v[30:33]
	v_mfma_f32_16x16x32_bf16 v[26:29], v[176:179], v[218:221], v[26:29]
	v_mfma_f32_16x16x32_bf16 v[14:17], v[160:163], v[226:229], v[14:17]
	v_mfma_f32_16x16x32_bf16 v[10:13], v[176:179], v[226:229], v[10:13]
	s_setprio 0
	s_setprio 1
	v_mfma_f32_16x16x32_bf16 v[54:57], v[172:175], v[192:195], 0
	v_mfma_f32_16x16x32_bf16 v[50:53], v[184:187], v[192:195], 0
	v_mfma_f32_16x16x32_bf16 v[38:41], v[172:175], v[200:203], 0
	v_mfma_f32_16x16x32_bf16 v[34:37], v[184:187], v[200:203], 0
	v_mfma_f32_16x16x32_bf16 v[22:25], v[172:175], v[214:217], 0
	v_mfma_f32_16x16x32_bf16 v[18:21], v[184:187], v[214:217], 0
	v_mfma_f32_16x16x32_bf16 v[6:9], v[172:175], v[222:225], 0
	v_mfma_f32_16x16x32_bf16 v[2:5], v[184:187], v[222:225], 0
	v_mfma_f32_16x16x32_bf16 v[54:57], v[180:183], v[196:199], v[54:57]
	v_mfma_f32_16x16x32_bf16 v[50:53], v[188:191], v[196:199], v[50:53]
	v_mfma_f32_16x16x32_bf16 v[38:41], v[180:183], v[204:207], v[38:41]
	v_mfma_f32_16x16x32_bf16 v[34:37], v[188:191], v[204:207], v[34:37]
	v_mfma_f32_16x16x32_bf16 v[22:25], v[180:183], v[218:221], v[22:25]
	v_mfma_f32_16x16x32_bf16 v[18:21], v[188:191], v[218:221], v[18:21]
	v_mfma_f32_16x16x32_bf16 v[6:9], v[180:183], v[226:229], v[6:9]
	v_mfma_f32_16x16x32_bf16 v[2:5], v[188:191], v[226:229], v[2:5]
	s_setprio 0
	s_barrier
	s_branch .Lmid_0
	.p2align 6

.LBB0_601:
	s_andn2_b64 vcc, exec, s[10:11]
	s_cbranch_vccnz .Lzs_1
	s_add_i32 s16, s74, 0x80
	s_addk_i32 s73, 0x100
	s_mov_b32 s74, 0
	ds_read_b128 v[164:167], v147
	ds_read_b128 v[168:171], v148
	ds_read_b128 v[172:175], v143
	ds_read_b128 v[176:179], v144
	ds_read_b128 v[180:183], v149
	ds_read_b128 v[184:187], v150
	ds_read_b128 v[188:191], v151
	ds_read_b128 v[192:195], v152
	s_add_i32 s75, s16, 0x80
	s_cmp_eq_u32 s59, s74
	s_cselect_b32 s76, s17, s73
	s_cselect_b32 s75, s72, s75
	v_add_u32_e32 v134, s16, v160
	s_add_i32 m0, s28, 0xc000
	ds_read_b128 v[196:199], v161
	ds_read_b128 v[200:203], v161 offset:1024
	ds_read_b128 v[204:207], v161 offset:2048
	ds_read_b128 v[214:217], v161 offset:3072
	ds_read_b128 v[218:221], v161 offset:4096
	ds_read_b128 v[222:225], v161 offset:5120
	ds_read_b128 v[226:229], v161 offset:6144
	ds_read_b128 v[230:233], v161 offset:7168
	global_load_lds_dwordx4 v134, s[4:5]
	v_add_u32_e32 v134, s16, v159
	s_add_i32 m0, s28, 0xe000
	s_nop 0
	global_load_lds_dwordx4 v134, s[4:5]
	s_waitcnt vmcnt(8)
	s_waitcnt lgkmcnt(0)
	s_barrier
	s_setprio 1
	s_waitcnt lgkmcnt(0)
	v_mfma_f32_16x16x32_bf16 v[126:129], v[172:175], v[196:199], 0
	v_mfma_f32_16x16x32_bf16 v[122:125], v[168:171], v[196:199], 0
	v_mfma_f32_16x16x32_bf16 v[110:113], v[172:175], v[204:207], 0
	v_mfma_f32_16x16x32_bf16 v[106:109], v[168:171], v[204:207], 0
	v_mfma_f32_16x16x32_bf16 v[94:97], v[172:175], v[218:221], 0
	v_mfma_f32_16x16x32_bf16 v[90:93], v[168:171], v[218:221], 0
	v_mfma_f32_16x16x32_bf16 v[78:81], v[172:175], v[226:229], 0
	v_mfma_f32_16x16x32_bf16 v[74:77], v[168:171], v[226:229], 0
	v_mfma_f32_16x16x32_bf16 v[126:129], v[164:167], v[200:203], v[126:129]
	v_mfma_f32_16x16x32_bf16 v[122:125], v[180:183], v[200:203], v[122:125]
	v_mfma_f32_16x16x32_bf16 v[110:113], v[164:167], v[214:217], v[110:113]
	v_mfma_f32_16x16x32_bf16 v[106:109], v[180:183], v[214:217], v[106:109]
	v_mfma_f32_16x16x32_bf16 v[94:97], v[164:167], v[222:225], v[94:97]
	v_mfma_f32_16x16x32_bf16 v[90:93], v[180:183], v[222:225], v[90:93]
	v_mfma_f32_16x16x32_bf16 v[78:81], v[164:167], v[230:233], v[78:81]
	v_mfma_f32_16x16x32_bf16 v[74:77], v[180:183], v[230:233], v[74:77]
	s_setprio 0
	s_setprio 1
	v_mfma_f32_16x16x32_bf16 v[118:121], v[176:179], v[196:199], 0
	v_mfma_f32_16x16x32_bf16 v[114:117], v[188:191], v[196:199], 0
	v_mfma_f32_16x16x32_bf16 v[102:105], v[176:179], v[204:207], 0
	v_mfma_f32_16x16x32_bf16 v[98:101], v[188:191], v[204:207], 0
	v_mfma_f32_16x16x32_bf16 v[86:89], v[176:179], v[218:221], 0
	v_mfma_f32_16x16x32_bf16 v[82:85], v[188:191], v[218:221], 0
	v_mfma_f32_16x16x32_bf16 v[70:73], v[176:179], v[226:229], 0
	v_mfma_f32_16x16x32_bf16 v[66:69], v[188:191], v[226:229], 0
	v_mfma_f32_16x16x32_bf16 v[118:121], v[184:187], v[200:203], v[118:121]
	v_mfma_f32_16x16x32_bf16 v[114:117], v[192:195], v[200:203], v[114:117]
	v_mfma_f32_16x16x32_bf16 v[102:105], v[184:187], v[214:217], v[102:105]
	v_mfma_f32_16x16x32_bf16 v[98:101], v[192:195], v[214:217], v[98:101]
	v_mfma_f32_16x16x32_bf16 v[86:89], v[184:187], v[222:225], v[86:89]
	v_mfma_f32_16x16x32_bf16 v[82:85], v[192:195], v[222:225], v[82:85]
	v_mfma_f32_16x16x32_bf16 v[70:73], v[184:187], v[230:233], v[70:73]
	v_mfma_f32_16x16x32_bf16 v[66:69], v[192:195], v[230:233], v[66:69]
	s_setprio 0
	s_barrier
	s_mov_b32 m0, s29
	v_add_u32_e32 v134, s76, v135
	ds_read_b128 v[196:199], v161 offset:16384
	ds_read_b128 v[200:203], v161 offset:17408
	ds_read_b128 v[204:207], v161 offset:18432
	ds_read_b128 v[214:217], v161 offset:19456
	ds_read_b128 v[218:221], v161 offset:20480
	ds_read_b128 v[222:225], v161 offset:21504
	ds_read_b128 v[226:229], v161 offset:22528
	ds_read_b128 v[230:233], v161 offset:23552
	global_load_lds_dwordx4 v134, s[6:7]
	v_add_u32_e32 v134, s23, v134
	s_mov_b32 m0, s30
	s_nop 0
	global_load_lds_dwordx4 v134, s[6:7]
	v_add_u32_e32 v134, s76, v138
	s_mov_b32 m0, s31
	s_nop 0
	global_load_lds_dwordx4 v134, s[6:7]
	v_add_u32_e32 v134, s23, v134
	s_mov_b32 m0, s35
	s_nop 0
	global_load_lds_dwordx4 v134, s[6:7]
	v_add_u32_e32 v134, s75, v1
	s_mov_b32 m0, s28
	s_nop 0
	global_load_lds_dwordx4 v134, s[4:5]
	v_add_u32_e32 v134, s22, v134
	s_mov_b32 m0, s44
	s_nop 0
	global_load_lds_dwordx4 v134, s[4:5]
	s_waitcnt vmcnt(8)
	s_waitcnt lgkmcnt(0)
	s_barrier
	s_setprio 1
	s_waitcnt lgkmcnt(0)
	v_mfma_f32_16x16x32_bf16 v[62:65], v[172:175], v[196:199], 0
	v_mfma_f32_16x16x32_bf16 v[58:61], v[168:171], v[196:199], 0
	v_mfma_f32_16x16x32_bf16 v[46:49], v[172:175], v[204:207], 0
	v_mfma_f32_16x16x32_bf16 v[42:45], v[168:171], v[204:207], 0
	v_mfma_f32_16x16x32_bf16 v[30:33], v[172:175], v[218:221], 0
	v_mfma_f32_16x16x32_bf16 v[26:29], v[168:171], v[218:221], 0
	v_mfma_f32_16x16x32_bf16 v[14:17], v[172:175], v[226:229], 0
	v_mfma_f32_16x16x32_bf16 v[10:13], v[168:171], v[226:229], 0
	v_mfma_f32_16x16x32_bf16 v[62:65], v[164:167], v[200:203], v[62:65]
	v_mfma_f32_16x16x32_bf16 v[58:61], v[180:183], v[200:203], v[58:61]
	v_mfma_f32_16x16x32_bf16 v[46:49], v[164:167], v[214:217], v[46:49]
	v_mfma_f32_16x16x32_bf16 v[42:45], v[180:183], v[214:217], v[42:45]
	v_mfma_f32_16x16x32_bf16 v[30:33], v[164:167], v[222:225], v[30:33]
	v_mfma_f32_16x16x32_bf16 v[26:29], v[180:183], v[222:225], v[26:29]
	v_mfma_f32_16x16x32_bf16 v[14:17], v[164:167], v[230:233], v[14:17]
	v_mfma_f32_16x16x32_bf16 v[10:13], v[180:183], v[230:233], v[10:13]
	s_setprio 0
	s_setprio 1
	v_mfma_f32_16x16x32_bf16 v[54:57], v[176:179], v[196:199], 0
	v_mfma_f32_16x16x32_bf16 v[50:53], v[188:191], v[196:199], 0
	v_mfma_f32_16x16x32_bf16 v[38:41], v[176:179], v[204:207], 0
	v_mfma_f32_16x16x32_bf16 v[34:37], v[188:191], v[204:207], 0
	v_mfma_f32_16x16x32_bf16 v[22:25], v[176:179], v[218:221], 0
	v_mfma_f32_16x16x32_bf16 v[18:21], v[188:191], v[218:221], 0
	v_mfma_f32_16x16x32_bf16 v[6:9], v[176:179], v[226:229], 0
	v_mfma_f32_16x16x32_bf16 v[2:5], v[188:191], v[226:229], 0
	v_mfma_f32_16x16x32_bf16 v[54:57], v[184:187], v[200:203], v[54:57]
	v_mfma_f32_16x16x32_bf16 v[50:53], v[192:195], v[200:203], v[50:53]
	v_mfma_f32_16x16x32_bf16 v[38:41], v[184:187], v[214:217], v[38:41]
	v_mfma_f32_16x16x32_bf16 v[34:37], v[192:195], v[214:217], v[34:37]
	v_mfma_f32_16x16x32_bf16 v[22:25], v[184:187], v[222:225], v[22:25]
	v_mfma_f32_16x16x32_bf16 v[18:21], v[192:195], v[222:225], v[18:21]
	v_mfma_f32_16x16x32_bf16 v[6:9], v[184:187], v[230:233], v[6:9]
	v_mfma_f32_16x16x32_bf16 v[2:5], v[192:195], v[230:233], v[2:5]
	s_setprio 0
	s_barrier
	s_branch .Lmid_1
	.p2align 6

.LBB0_618:
	s_andn2_b64 vcc, exec, s[10:11]
	s_cbranch_vccnz .Lzs_2
	s_add_i32 s16, s72, 0x80
	s_addk_i32 s71, 0x100
	s_mov_b32 s72, 0
	ds_read_b128 v[160:163], v144
	ds_read_b128 v[164:167], v145
	ds_read_b128 v[168:171], v140
	ds_read_b128 v[172:175], v141
	ds_read_b128 v[176:179], v146
	ds_read_b128 v[180:183], v147
	ds_read_b128 v[184:187], v148
	ds_read_b128 v[188:191], v149
	s_add_i32 s73, s16, 0x80
	s_cmp_eq_u32 s20, s72
	s_cselect_b32 s74, s15, s71
	s_cselect_b32 s73, s17, s73
	v_add_u32_e32 v159, s16, v157
	s_add_i32 m0, s28, 0xc000
	ds_read_b128 v[192:195], v158
	ds_read_b128 v[196:199], v158 offset:1024
	ds_read_b128 v[200:203], v158 offset:2048
	ds_read_b128 v[204:207], v158 offset:3072
	ds_read_b128 v[214:217], v158 offset:4096
	ds_read_b128 v[218:221], v158 offset:5120
	ds_read_b128 v[222:225], v158 offset:6144
	ds_read_b128 v[226:229], v158 offset:7168
	global_load_lds_dwordx4 v159, s[4:5]
	v_add_u32_e32 v159, s16, v156
	s_add_i32 m0, s28, 0xe000
	s_nop 0
	global_load_lds_dwordx4 v159, s[4:5]
	s_waitcnt vmcnt(8)
	s_waitcnt lgkmcnt(0)
	s_barrier
	s_setprio 1
	s_waitcnt lgkmcnt(0)
	v_mfma_f32_16x16x32_bf16 v[122:125], v[168:171], v[192:195], 0
	v_mfma_f32_16x16x32_bf16 v[126:129], v[164:167], v[192:195], 0
	v_mfma_f32_16x16x32_bf16 v[110:113], v[168:171], v[200:203], 0
	v_mfma_f32_16x16x32_bf16 v[106:109], v[164:167], v[200:203], 0
	v_mfma_f32_16x16x32_bf16 v[94:97], v[168:171], v[214:217], 0
	v_mfma_f32_16x16x32_bf16 v[90:93], v[164:167], v[214:217], 0
	v_mfma_f32_16x16x32_bf16 v[78:81], v[168:171], v[222:225], 0
	v_mfma_f32_16x16x32_bf16 v[74:77], v[164:167], v[222:225], 0
	v_mfma_f32_16x16x32_bf16 v[122:125], v[160:163], v[196:199], v[122:125]
	v_mfma_f32_16x16x32_bf16 v[126:129], v[176:179], v[196:199], v[126:129]
	v_mfma_f32_16x16x32_bf16 v[110:113], v[160:163], v[204:207], v[110:113]
	v_mfma_f32_16x16x32_bf16 v[106:109], v[176:179], v[204:207], v[106:109]
	v_mfma_f32_16x16x32_bf16 v[94:97], v[160:163], v[218:221], v[94:97]
	v_mfma_f32_16x16x32_bf16 v[90:93], v[176:179], v[218:221], v[90:93]
	v_mfma_f32_16x16x32_bf16 v[78:81], v[160:163], v[226:229], v[78:81]
	v_mfma_f32_16x16x32_bf16 v[74:77], v[176:179], v[226:229], v[74:77]
	s_setprio 0
	s_setprio 1
	v_mfma_f32_16x16x32_bf16 v[118:121], v[172:175], v[192:195], 0
	v_mfma_f32_16x16x32_bf16 v[114:117], v[184:187], v[192:195], 0
	v_mfma_f32_16x16x32_bf16 v[102:105], v[172:175], v[200:203], 0
	v_mfma_f32_16x16x32_bf16 v[98:101], v[184:187], v[200:203], 0
	v_mfma_f32_16x16x32_bf16 v[86:89], v[172:175], v[214:217], 0
	v_mfma_f32_16x16x32_bf16 v[82:85], v[184:187], v[214:217], 0
	v_mfma_f32_16x16x32_bf16 v[70:73], v[172:175], v[222:225], 0
	v_mfma_f32_16x16x32_bf16 v[66:69], v[184:187], v[222:225], 0
	v_mfma_f32_16x16x32_bf16 v[118:121], v[180:183], v[196:199], v[118:121]
	v_mfma_f32_16x16x32_bf16 v[114:117], v[188:191], v[196:199], v[114:117]
	v_mfma_f32_16x16x32_bf16 v[102:105], v[180:183], v[204:207], v[102:105]
	v_mfma_f32_16x16x32_bf16 v[98:101], v[188:191], v[204:207], v[98:101]
	v_mfma_f32_16x16x32_bf16 v[86:89], v[180:183], v[218:221], v[86:89]
	v_mfma_f32_16x16x32_bf16 v[82:85], v[188:191], v[218:221], v[82:85]
	v_mfma_f32_16x16x32_bf16 v[70:73], v[180:183], v[226:229], v[70:73]
	v_mfma_f32_16x16x32_bf16 v[66:69], v[188:191], v[226:229], v[66:69]
	s_setprio 0
	s_barrier
	s_mov_b32 m0, s29
	v_add_u32_e32 v159, s74, v134
	ds_read_b128 v[192:195], v158 offset:16384
	ds_read_b128 v[196:199], v158 offset:17408
	ds_read_b128 v[200:203], v158 offset:18432
	ds_read_b128 v[204:207], v158 offset:19456
	ds_read_b128 v[214:217], v158 offset:20480
	ds_read_b128 v[218:221], v158 offset:21504
	ds_read_b128 v[222:225], v158 offset:22528
	ds_read_b128 v[226:229], v158 offset:23552
	global_load_lds_dwordx4 v159, s[6:7]
	v_add_u32_e32 v159, s23, v159
	s_mov_b32 m0, s30
	s_nop 0
	global_load_lds_dwordx4 v159, s[6:7]
	v_add_u32_e32 v159, s74, v135
	s_mov_b32 m0, s31
	s_nop 0
	global_load_lds_dwordx4 v159, s[6:7]
	v_add_u32_e32 v159, s23, v159
	s_mov_b32 m0, s35
	s_nop 0
	global_load_lds_dwordx4 v159, s[6:7]
	v_add_u32_e32 v159, s73, v1
	s_mov_b32 m0, s28
	s_nop 0
	global_load_lds_dwordx4 v159, s[4:5]
	v_add_u32_e32 v159, s22, v159
	s_mov_b32 m0, s44
	s_nop 0
	global_load_lds_dwordx4 v159, s[4:5]
	s_waitcnt vmcnt(8)
	s_waitcnt lgkmcnt(0)
	s_barrier
	s_setprio 1
	s_waitcnt lgkmcnt(0)
	v_mfma_f32_16x16x32_bf16 v[62:65], v[168:171], v[192:195], 0
	v_mfma_f32_16x16x32_bf16 v[58:61], v[164:167], v[192:195], 0
	v_mfma_f32_16x16x32_bf16 v[46:49], v[168:171], v[200:203], 0
	v_mfma_f32_16x16x32_bf16 v[42:45], v[164:167], v[200:203], 0
	v_mfma_f32_16x16x32_bf16 v[30:33], v[168:171], v[214:217], 0
	v_mfma_f32_16x16x32_bf16 v[26:29], v[164:167], v[214:217], 0
	v_mfma_f32_16x16x32_bf16 v[14:17], v[168:171], v[222:225], 0
	v_mfma_f32_16x16x32_bf16 v[10:13], v[164:167], v[222:225], 0
	v_mfma_f32_16x16x32_bf16 v[62:65], v[160:163], v[196:199], v[62:65]
	v_mfma_f32_16x16x32_bf16 v[58:61], v[176:179], v[196:199], v[58:61]
	v_mfma_f32_16x16x32_bf16 v[46:49], v[160:163], v[204:207], v[46:49]
	v_mfma_f32_16x16x32_bf16 v[42:45], v[176:179], v[204:207], v[42:45]
	v_mfma_f32_16x16x32_bf16 v[30:33], v[160:163], v[218:221], v[30:33]
	v_mfma_f32_16x16x32_bf16 v[26:29], v[176:179], v[218:221], v[26:29]
	v_mfma_f32_16x16x32_bf16 v[14:17], v[160:163], v[226:229], v[14:17]
	v_mfma_f32_16x16x32_bf16 v[10:13], v[176:179], v[226:229], v[10:13]
	s_setprio 0
	s_setprio 1
	v_mfma_f32_16x16x32_bf16 v[54:57], v[172:175], v[192:195], 0
	v_mfma_f32_16x16x32_bf16 v[50:53], v[184:187], v[192:195], 0
	v_mfma_f32_16x16x32_bf16 v[38:41], v[172:175], v[200:203], 0
	v_mfma_f32_16x16x32_bf16 v[34:37], v[184:187], v[200:203], 0
	v_mfma_f32_16x16x32_bf16 v[22:25], v[172:175], v[214:217], 0
	v_mfma_f32_16x16x32_bf16 v[18:21], v[184:187], v[214:217], 0
	v_mfma_f32_16x16x32_bf16 v[6:9], v[172:175], v[222:225], 0
	v_mfma_f32_16x16x32_bf16 v[2:5], v[184:187], v[222:225], 0
	v_mfma_f32_16x16x32_bf16 v[54:57], v[180:183], v[196:199], v[54:57]
	v_mfma_f32_16x16x32_bf16 v[50:53], v[188:191], v[196:199], v[50:53]
	v_mfma_f32_16x16x32_bf16 v[38:41], v[180:183], v[204:207], v[38:41]
	v_mfma_f32_16x16x32_bf16 v[34:37], v[188:191], v[204:207], v[34:37]
	v_mfma_f32_16x16x32_bf16 v[22:25], v[180:183], v[218:221], v[22:25]
	v_mfma_f32_16x16x32_bf16 v[18:21], v[188:191], v[218:221], v[18:21]
	v_mfma_f32_16x16x32_bf16 v[6:9], v[180:183], v[226:229], v[6:9]
	v_mfma_f32_16x16x32_bf16 v[2:5], v[188:191], v[226:229], v[2:5]
	s_setprio 0
	s_barrier
	s_branch .Lmid_2
	.p2align 6

.LBB0_635:
	s_andn2_b64 vcc, exec, s[20:21]
	s_cbranch_vccnz .Lzs_3
	s_add_i32 s28, s79, 0x80
	s_add_i32 s79, s75, 0x100
	s_mov_b32 s80, 0
	ds_read_b128 v[130:133], v188
	ds_read_b128 v[134:137], v189
	ds_read_b128 v[138:141], v184
	ds_read_b128 v[142:145], v185
	ds_read_b128 v[146:149], v190
	ds_read_b128 v[150:153], v191
	ds_read_b128 v[154:157], v192
	ds_read_b128 v[158:161], v193
	s_add_i32 s75, s28, 0x80
	s_cmp_eq_u32 s66, s80
	s_cselect_b32 s81, s25, s79
	s_cselect_b32 s75, s29, s75
	v_add_u32_e32 v203, s28, v201
	s_add_i32 m0, s46, 0xc000
	ds_read_b128 v[162:165], v202
	ds_read_b128 v[166:169], v202 offset:1024
	ds_read_b128 v[170:173], v202 offset:2048
	ds_read_b128 v[204:207], v202 offset:3072
	ds_read_b128 v[214:217], v202 offset:4096
	ds_read_b128 v[218:221], v202 offset:5120
	ds_read_b128 v[222:225], v202 offset:6144
	ds_read_b128 v[226:229], v202 offset:7168
	global_load_lds_dwordx4 v203, s[4:5]
	v_add_u32_e32 v203, s28, v200
	s_add_i32 m0, s46, 0xe000
	s_nop 0
	global_load_lds_dwordx4 v203, s[4:5]
	s_waitcnt vmcnt(8)
	s_waitcnt lgkmcnt(0)
	s_barrier
	s_setprio 1
	s_waitcnt lgkmcnt(0)
	v_mfma_f32_16x16x32_bf16 v[126:129], v[138:141], v[162:165], 0
	v_mfma_f32_16x16x32_bf16 v[118:121], v[134:137], v[162:165], 0
	v_mfma_f32_16x16x32_bf16 v[110:113], v[138:141], v[170:173], 0
	v_mfma_f32_16x16x32_bf16 v[102:105], v[134:137], v[170:173], 0
	v_mfma_f32_16x16x32_bf16 v[94:97], v[138:141], v[214:217], 0
	v_mfma_f32_16x16x32_bf16 v[86:89], v[134:137], v[214:217], 0
	v_mfma_f32_16x16x32_bf16 v[78:81], v[138:141], v[222:225], 0
	v_mfma_f32_16x16x32_bf16 v[70:73], v[134:137], v[222:225], 0
	v_mfma_f32_16x16x32_bf16 v[126:129], v[130:133], v[166:169], v[126:129]
	v_mfma_f32_16x16x32_bf16 v[118:121], v[146:149], v[166:169], v[118:121]
	v_mfma_f32_16x16x32_bf16 v[110:113], v[130:133], v[204:207], v[110:113]
	v_mfma_f32_16x16x32_bf16 v[102:105], v[146:149], v[204:207], v[102:105]
	v_mfma_f32_16x16x32_bf16 v[94:97], v[130:133], v[218:221], v[94:97]
	v_mfma_f32_16x16x32_bf16 v[86:89], v[146:149], v[218:221], v[86:89]
	v_mfma_f32_16x16x32_bf16 v[78:81], v[130:133], v[226:229], v[78:81]
	v_mfma_f32_16x16x32_bf16 v[70:73], v[146:149], v[226:229], v[70:73]
	s_setprio 0
	s_setprio 1
	v_mfma_f32_16x16x32_bf16 v[122:125], v[142:145], v[162:165], 0
	v_mfma_f32_16x16x32_bf16 v[114:117], v[154:157], v[162:165], 0
	v_mfma_f32_16x16x32_bf16 v[106:109], v[142:145], v[170:173], 0
	v_mfma_f32_16x16x32_bf16 v[98:101], v[154:157], v[170:173], 0
	v_mfma_f32_16x16x32_bf16 v[90:93], v[142:145], v[214:217], 0
	v_mfma_f32_16x16x32_bf16 v[82:85], v[154:157], v[214:217], 0
	v_mfma_f32_16x16x32_bf16 v[74:77], v[142:145], v[222:225], 0
	v_mfma_f32_16x16x32_bf16 v[66:69], v[154:157], v[222:225], 0
	v_mfma_f32_16x16x32_bf16 v[122:125], v[150:153], v[166:169], v[122:125]
	v_mfma_f32_16x16x32_bf16 v[114:117], v[158:161], v[166:169], v[114:117]
	v_mfma_f32_16x16x32_bf16 v[106:109], v[150:153], v[204:207], v[106:109]
	v_mfma_f32_16x16x32_bf16 v[98:101], v[158:161], v[204:207], v[98:101]
	v_mfma_f32_16x16x32_bf16 v[90:93], v[150:153], v[218:221], v[90:93]
	v_mfma_f32_16x16x32_bf16 v[82:85], v[158:161], v[218:221], v[82:85]
	v_mfma_f32_16x16x32_bf16 v[74:77], v[150:153], v[226:229], v[74:77]
	v_mfma_f32_16x16x32_bf16 v[66:69], v[158:161], v[226:229], v[66:69]
	s_setprio 0
	s_barrier
	s_mov_b32 m0, s47
	v_add_u32_e32 v203, s81, v178
	ds_read_b128 v[162:165], v202 offset:16384
	ds_read_b128 v[166:169], v202 offset:17408
	ds_read_b128 v[170:173], v202 offset:18432
	ds_read_b128 v[204:207], v202 offset:19456
	ds_read_b128 v[214:217], v202 offset:20480
	ds_read_b128 v[218:221], v202 offset:21504
	ds_read_b128 v[222:225], v202 offset:22528
	ds_read_b128 v[226:229], v202 offset:23552
	global_load_lds_dwordx4 v203, s[6:7]
	v_add_u32_e32 v203, s35, v203
	s_mov_b32 m0, s48
	s_nop 0
	global_load_lds_dwordx4 v203, s[6:7]
	v_add_u32_e32 v203, s81, v179
	s_mov_b32 m0, s49
	s_nop 0
	global_load_lds_dwordx4 v203, s[6:7]
	v_add_u32_e32 v203, s35, v203
	s_mov_b32 m0, s50
	s_nop 0
	global_load_lds_dwordx4 v203, s[6:7]
	v_add_u32_e32 v203, s75, v1
	s_mov_b32 m0, s46
	s_nop 0
	global_load_lds_dwordx4 v203, s[4:5]
	v_add_u32_e32 v203, s31, v203
	s_mov_b32 m0, s51
	s_nop 0
	global_load_lds_dwordx4 v203, s[4:5]
	s_waitcnt vmcnt(8)
	s_waitcnt lgkmcnt(0)
	s_barrier
	s_setprio 1
	s_waitcnt lgkmcnt(0)
	v_mfma_f32_16x16x32_bf16 v[62:65], v[138:141], v[162:165], 0
	v_mfma_f32_16x16x32_bf16 v[54:57], v[134:137], v[162:165], 0
	v_mfma_f32_16x16x32_bf16 v[46:49], v[138:141], v[170:173], 0
	v_mfma_f32_16x16x32_bf16 v[38:41], v[134:137], v[170:173], 0
	v_mfma_f32_16x16x32_bf16 v[30:33], v[138:141], v[214:217], 0
	v_mfma_f32_16x16x32_bf16 v[22:25], v[134:137], v[214:217], 0
	v_mfma_f32_16x16x32_bf16 v[14:17], v[138:141], v[222:225], 0
	v_mfma_f32_16x16x32_bf16 v[6:9], v[134:137], v[222:225], 0
	v_mfma_f32_16x16x32_bf16 v[62:65], v[130:133], v[166:169], v[62:65]
	v_mfma_f32_16x16x32_bf16 v[54:57], v[146:149], v[166:169], v[54:57]
	v_mfma_f32_16x16x32_bf16 v[46:49], v[130:133], v[204:207], v[46:49]
	v_mfma_f32_16x16x32_bf16 v[38:41], v[146:149], v[204:207], v[38:41]
	v_mfma_f32_16x16x32_bf16 v[30:33], v[130:133], v[218:221], v[30:33]
	v_mfma_f32_16x16x32_bf16 v[22:25], v[146:149], v[218:221], v[22:25]
	v_mfma_f32_16x16x32_bf16 v[14:17], v[130:133], v[226:229], v[14:17]
	v_mfma_f32_16x16x32_bf16 v[6:9], v[146:149], v[226:229], v[6:9]
	s_setprio 0
	s_setprio 1
	v_mfma_f32_16x16x32_bf16 v[58:61], v[142:145], v[162:165], 0
	v_mfma_f32_16x16x32_bf16 v[50:53], v[154:157], v[162:165], 0
	v_mfma_f32_16x16x32_bf16 v[42:45], v[142:145], v[170:173], 0
	v_mfma_f32_16x16x32_bf16 v[34:37], v[154:157], v[170:173], 0
	v_mfma_f32_16x16x32_bf16 v[26:29], v[142:145], v[214:217], 0
	v_mfma_f32_16x16x32_bf16 v[18:21], v[154:157], v[214:217], 0
	v_mfma_f32_16x16x32_bf16 v[10:13], v[142:145], v[222:225], 0
	v_mfma_f32_16x16x32_bf16 v[2:5], v[154:157], v[222:225], 0
	v_mfma_f32_16x16x32_bf16 v[58:61], v[150:153], v[166:169], v[58:61]
	v_mfma_f32_16x16x32_bf16 v[50:53], v[158:161], v[166:169], v[50:53]
	v_mfma_f32_16x16x32_bf16 v[42:45], v[150:153], v[204:207], v[42:45]
	v_mfma_f32_16x16x32_bf16 v[34:37], v[158:161], v[204:207], v[34:37]
	v_mfma_f32_16x16x32_bf16 v[26:29], v[150:153], v[218:221], v[26:29]
	v_mfma_f32_16x16x32_bf16 v[18:21], v[158:161], v[218:221], v[18:21]
	v_mfma_f32_16x16x32_bf16 v[10:13], v[150:153], v[226:229], v[10:13]
	v_mfma_f32_16x16x32_bf16 v[2:5], v[158:161], v[226:229], v[2:5]
	s_setprio 0
	s_barrier
	s_branch .Lmid_3
	.p2align 6

.LBB0_1181:
	s_andn2_b64 vcc, exec, s[16:17]
	s_waitcnt lgkmcnt(0)
	s_cbranch_vccnz .Lzs_4
	s_add_i32 s6, s58, 0x80
	s_add_i32 s58, s59, 0x100
	s_mov_b32 s59, 0
	ds_read_b128 v[114:117], v206
	ds_read_b128 v[118:121], v207
	ds_read_b128 v[122:125], v202
	ds_read_b128 v[126:129], v203
	ds_read_b128 v[146:149], v208
	ds_read_b128 v[150:153], v209
	ds_read_b128 v[154:157], v211
	ds_read_b128 v[158:161], v213
	s_add_i32 s60, s6, 0x80
	s_cmp_eq_u32 s90, s59
	s_cselect_b32 s61, s5, s58
	s_cselect_b32 s60, s7, s60
	v_add_u32_e32 v194, s6, v221
	s_add_i32 m0, s70, 0xc000
	ds_read_b128 v[162:165], v222
	ds_read_b128 v[170:173], v222 offset:1024
	ds_read_b128 v[174:177], v222 offset:2048
	ds_read_b128 v[178:181], v222 offset:3072
	ds_read_b128 v[182:185], v222 offset:4096
	ds_read_b128 v[186:189], v222 offset:5120
	ds_read_b128 v[190:193], v222 offset:6144
	ds_read_b128 v[226:229], v222 offset:7168
	global_load_lds_dwordx4 v194, s[8:9]
	v_add_u32_e32 v194, s6, v220
	s_add_i32 m0, s70, 0xe000
	s_nop 0
	global_load_lds_dwordx4 v194, s[8:9]
	s_waitcnt vmcnt(8)
	s_waitcnt lgkmcnt(0)
	s_barrier
	s_setprio 1
	s_waitcnt lgkmcnt(0)
	v_mfma_f32_16x16x32_bf16 v[142:145], v[122:125], v[162:165], 0
	v_mfma_f32_16x16x32_bf16 v[138:141], v[118:121], v[162:165], 0
	v_mfma_f32_16x16x32_bf16 v[110:113], v[122:125], v[174:177], 0
	v_mfma_f32_16x16x32_bf16 v[106:109], v[118:121], v[174:177], 0
	v_mfma_f32_16x16x32_bf16 v[94:97], v[122:125], v[182:185], 0
	v_mfma_f32_16x16x32_bf16 v[90:93], v[118:121], v[182:185], 0
	v_mfma_f32_16x16x32_bf16 v[78:81], v[122:125], v[190:193], 0
	v_mfma_f32_16x16x32_bf16 v[74:77], v[118:121], v[190:193], 0
	v_mfma_f32_16x16x32_bf16 v[142:145], v[114:117], v[170:173], v[142:145]
	v_mfma_f32_16x16x32_bf16 v[138:141], v[146:149], v[170:173], v[138:141]
	v_mfma_f32_16x16x32_bf16 v[110:113], v[114:117], v[178:181], v[110:113]
	v_mfma_f32_16x16x32_bf16 v[106:109], v[146:149], v[178:181], v[106:109]
	v_mfma_f32_16x16x32_bf16 v[94:97], v[114:117], v[186:189], v[94:97]
	v_mfma_f32_16x16x32_bf16 v[90:93], v[146:149], v[186:189], v[90:93]
	v_mfma_f32_16x16x32_bf16 v[78:81], v[114:117], v[226:229], v[78:81]
	v_mfma_f32_16x16x32_bf16 v[74:77], v[146:149], v[226:229], v[74:77]
	s_setprio 0
	s_setprio 1
	v_mfma_f32_16x16x32_bf16 v[134:137], v[126:129], v[162:165], 0
	v_mfma_f32_16x16x32_bf16 v[130:133], v[154:157], v[162:165], 0
	v_mfma_f32_16x16x32_bf16 v[102:105], v[126:129], v[174:177], 0
	v_mfma_f32_16x16x32_bf16 v[98:101], v[154:157], v[174:177], 0
	v_mfma_f32_16x16x32_bf16 v[86:89], v[126:129], v[182:185], 0
	v_mfma_f32_16x16x32_bf16 v[82:85], v[154:157], v[182:185], 0
	v_mfma_f32_16x16x32_bf16 v[70:73], v[126:129], v[190:193], 0
	v_mfma_f32_16x16x32_bf16 v[66:69], v[154:157], v[190:193], 0
	v_mfma_f32_16x16x32_bf16 v[134:137], v[150:153], v[170:173], v[134:137]
	v_mfma_f32_16x16x32_bf16 v[130:133], v[158:161], v[170:173], v[130:133]
	v_mfma_f32_16x16x32_bf16 v[102:105], v[150:153], v[178:181], v[102:105]
	v_mfma_f32_16x16x32_bf16 v[98:101], v[158:161], v[178:181], v[98:101]
	v_mfma_f32_16x16x32_bf16 v[86:89], v[150:153], v[186:189], v[86:89]
	v_mfma_f32_16x16x32_bf16 v[82:85], v[158:161], v[186:189], v[82:85]
	v_mfma_f32_16x16x32_bf16 v[70:73], v[150:153], v[226:229], v[70:73]
	v_mfma_f32_16x16x32_bf16 v[66:69], v[158:161], v[226:229], v[66:69]
	s_setprio 0
	s_barrier
	s_mov_b32 m0, s71
	v_add_u32_e32 v194, s61, v196
	ds_read_b128 v[162:165], v222 offset:16384
	ds_read_b128 v[170:173], v222 offset:17408
	ds_read_b128 v[174:177], v222 offset:18432
	ds_read_b128 v[178:181], v222 offset:19456
	ds_read_b128 v[182:185], v222 offset:20480
	ds_read_b128 v[186:189], v222 offset:21504
	ds_read_b128 v[190:193], v222 offset:22528
	ds_read_b128 v[226:229], v222 offset:23552
	global_load_lds_dwordx4 v194, s[20:21]
	v_add_u32_e32 v194, s35, v194
	s_mov_b32 m0, s72
	s_nop 0
	global_load_lds_dwordx4 v194, s[20:21]
	v_add_u32_e32 v194, s61, v197
	s_mov_b32 m0, s73
	s_nop 0
	global_load_lds_dwordx4 v194, s[20:21]
	v_add_u32_e32 v194, s35, v194
	s_mov_b32 m0, s76
	s_nop 0
	global_load_lds_dwordx4 v194, s[20:21]
	v_add_u32_e32 v194, s60, v1
	s_mov_b32 m0, s70
	s_nop 0
	global_load_lds_dwordx4 v194, s[8:9]
	v_add_u32_e32 v194, s29, v194
	s_mov_b32 m0, s77
	s_nop 0
	global_load_lds_dwordx4 v194, s[8:9]
	s_waitcnt vmcnt(8)
	s_waitcnt lgkmcnt(0)
	s_barrier
	s_setprio 1
	s_waitcnt lgkmcnt(0)
	v_mfma_f32_16x16x32_bf16 v[62:65], v[122:125], v[162:165], 0
	v_mfma_f32_16x16x32_bf16 v[58:61], v[118:121], v[162:165], 0
	v_mfma_f32_16x16x32_bf16 v[46:49], v[122:125], v[174:177], 0
	v_mfma_f32_16x16x32_bf16 v[42:45], v[118:121], v[174:177], 0
	v_mfma_f32_16x16x32_bf16 v[30:33], v[122:125], v[182:185], 0
	v_mfma_f32_16x16x32_bf16 v[26:29], v[118:121], v[182:185], 0
	v_mfma_f32_16x16x32_bf16 v[14:17], v[122:125], v[190:193], 0
	v_mfma_f32_16x16x32_bf16 v[10:13], v[118:121], v[190:193], 0
	v_mfma_f32_16x16x32_bf16 v[62:65], v[114:117], v[170:173], v[62:65]
	v_mfma_f32_16x16x32_bf16 v[58:61], v[146:149], v[170:173], v[58:61]
	v_mfma_f32_16x16x32_bf16 v[46:49], v[114:117], v[178:181], v[46:49]
	v_mfma_f32_16x16x32_bf16 v[42:45], v[146:149], v[178:181], v[42:45]
	v_mfma_f32_16x16x32_bf16 v[30:33], v[114:117], v[186:189], v[30:33]
	v_mfma_f32_16x16x32_bf16 v[26:29], v[146:149], v[186:189], v[26:29]
	v_mfma_f32_16x16x32_bf16 v[14:17], v[114:117], v[226:229], v[14:17]
	v_mfma_f32_16x16x32_bf16 v[10:13], v[146:149], v[226:229], v[10:13]
	s_setprio 0
	s_setprio 1
	v_mfma_f32_16x16x32_bf16 v[54:57], v[126:129], v[162:165], 0
	v_mfma_f32_16x16x32_bf16 v[50:53], v[154:157], v[162:165], 0
	v_mfma_f32_16x16x32_bf16 v[38:41], v[126:129], v[174:177], 0
	v_mfma_f32_16x16x32_bf16 v[34:37], v[154:157], v[174:177], 0
	v_mfma_f32_16x16x32_bf16 v[22:25], v[126:129], v[182:185], 0
	v_mfma_f32_16x16x32_bf16 v[18:21], v[154:157], v[182:185], 0
	v_mfma_f32_16x16x32_bf16 v[6:9], v[126:129], v[190:193], 0
	v_mfma_f32_16x16x32_bf16 v[2:5], v[154:157], v[190:193], 0
	v_mfma_f32_16x16x32_bf16 v[54:57], v[150:153], v[170:173], v[54:57]
	v_mfma_f32_16x16x32_bf16 v[50:53], v[158:161], v[170:173], v[50:53]
	v_mfma_f32_16x16x32_bf16 v[38:41], v[150:153], v[178:181], v[38:41]
	v_mfma_f32_16x16x32_bf16 v[34:37], v[158:161], v[178:181], v[34:37]
	v_mfma_f32_16x16x32_bf16 v[22:25], v[150:153], v[186:189], v[22:25]
	v_mfma_f32_16x16x32_bf16 v[18:21], v[158:161], v[186:189], v[18:21]
	v_mfma_f32_16x16x32_bf16 v[6:9], v[150:153], v[226:229], v[6:9]
	v_mfma_f32_16x16x32_bf16 v[2:5], v[158:161], v[226:229], v[2:5]
	s_setprio 0
	s_barrier
	s_branch .Lmid_4
	.p2align 6

.Lphr_0:
	ds_read_b128 v[18:21], v177
	ds_read_b128 v[22:25], v178
	ds_read_b128 v[26:29], v185
	ds_read_b128 v[30:33], v186
	ds_read_b128 v[2:5], v179
	ds_read_b128 v[6:9], v180
	ds_read_b128 v[10:13], v187
	ds_read_b128 v[14:17], v188
	s_add_i32 s75, s92, 0x80
	s_and_b64 s[30:31], s[30:31], exec
	s_cselect_b32 s75, s75, s91
	s_cselect_b32 s96, s93, s29
	s_add_i32 s30, s75, 0x80
	s_add_i32 s31, s96, 0x80
	v_mov_b32_e32 v162, v1
	ds_read_b128 v[198:201], v193
	ds_read_b128 v[202:205], v193 offset:1024
	ds_read_b128 v[214:217], v193 offset:2048
	ds_read_b128 v[218:221], v193 offset:3072
	ds_read_b128 v[222:225], v193 offset:4096
	ds_read_b128 v[226:229], v193 offset:5120
	ds_read_b128 v[230:233], v193 offset:6144
	ds_read_b128 v[234:237], v193 offset:7168
	s_add_i32 s97, s92, s65
	v_add_u32_e32 v162, s97, v162
	s_add_i32 m0, s47, 0xc000
	s_add_i32 s97, s92, s74
	global_load_lds_dwordx4 v162, s[10:11]
	v_mov_b32_e32 v162, v1
	s_add_i32 m0, s47, 0xe000
	v_add_u32_e32 v162, s97, v162
	global_load_lds_dwordx4 v162, s[10:11]
	s_waitcnt vmcnt(8)
	s_waitcnt lgkmcnt(0)
	s_barrier
	s_setprio 1
	s_waitcnt lgkmcnt(0)
	v_mfma_f32_16x16x128_f8f6f4 v[158:161], v[18:25], v[198:205], 0
	v_mfma_f32_16x16x128_f8f6f4 v[150:153], v[26:33], v[198:205], 0
	v_mfma_f32_16x16x128_f8f6f4 v[142:145], v[18:25], v[214:221], 0
	v_mfma_f32_16x16x128_f8f6f4 v[134:137], v[26:33], v[214:221], 0
	v_mfma_f32_16x16x128_f8f6f4 v[126:129], v[18:25], v[222:229], 0
	v_mfma_f32_16x16x128_f8f6f4 v[118:121], v[26:33], v[222:229], 0
	v_mfma_f32_16x16x128_f8f6f4 v[110:113], v[18:25], v[230:237], 0
	v_mfma_f32_16x16x128_f8f6f4 v[102:105], v[26:33], v[230:237], 0
	s_setprio 0
	s_setprio 1
	v_mfma_f32_16x16x128_f8f6f4 v[154:157], v[2:9], v[198:205], 0
	v_mfma_f32_16x16x128_f8f6f4 v[146:149], v[10:17], v[198:205], 0
	v_mfma_f32_16x16x128_f8f6f4 v[138:141], v[2:9], v[214:221], 0
	v_mfma_f32_16x16x128_f8f6f4 v[130:133], v[10:17], v[214:221], 0
	v_mfma_f32_16x16x128_f8f6f4 v[122:125], v[2:9], v[222:229], 0
	v_mfma_f32_16x16x128_f8f6f4 v[114:117], v[10:17], v[222:229], 0
	v_mfma_f32_16x16x128_f8f6f4 v[106:109], v[2:9], v[230:237], 0
	v_mfma_f32_16x16x128_f8f6f4 v[98:101], v[10:17], v[230:237], 0
	s_setprio 0
	s_barrier
	v_mov_b32_e32 v162, v174
	ds_read_b128 v[198:201], v193 offset:16384
	ds_read_b128 v[202:205], v193 offset:17408
	ds_read_b128 v[214:217], v193 offset:18432
	ds_read_b128 v[218:221], v193 offset:19456
	ds_read_b128 v[222:225], v193 offset:20480
	ds_read_b128 v[226:229], v193 offset:21504
	ds_read_b128 v[230:233], v193 offset:22528
	ds_read_b128 v[234:237], v193 offset:23552
	s_mov_b32 m0, s48
	v_add_u32_e32 v162, s96, v162
	global_load_lds_dwordx4 v162, s[20:21]
	v_mov_b32_e32 v162, v174
	s_add_i32 s96, s96, s46
	v_add_u32_e32 v162, s96, v162
	s_mov_b32 m0, s49
	s_add_i32 s96, s96, s46
	global_load_lds_dwordx4 v162, s[20:21]
	v_mov_b32_e32 v162, v174
	s_mov_b32 m0, s50
	v_add_u32_e32 v162, s96, v162
	global_load_lds_dwordx4 v162, s[20:21]
	v_mov_b32_e32 v162, v174
	s_add_i32 s96, s96, s46
	v_add_u32_e32 v162, s96, v162
	s_mov_b32 m0, s51
	s_nop 0
	global_load_lds_dwordx4 v162, s[20:21]
	v_mov_b32_e32 v162, v1
	s_mov_b32 m0, s47
	v_add_u32_e32 v162, s75, v162
	global_load_lds_dwordx4 v162, s[10:11]
	v_mov_b32_e32 v162, v1
	s_add_i32 s75, s75, s45
	v_add_u32_e32 v162, s75, v162
	s_mov_b32 m0, s52
	s_nop 0
	global_load_lds_dwordx4 v162, s[10:11]
	s_waitcnt vmcnt(8)
	s_waitcnt lgkmcnt(0)
	s_barrier
	s_setprio 1
	s_waitcnt lgkmcnt(0)
	v_mfma_f32_16x16x128_f8f6f4 v[94:97], v[18:25], v[198:205], 0
	v_mfma_f32_16x16x128_f8f6f4 v[86:89], v[26:33], v[198:205], 0
	v_mfma_f32_16x16x128_f8f6f4 v[78:81], v[18:25], v[214:221], 0
	v_mfma_f32_16x16x128_f8f6f4 v[70:73], v[26:33], v[214:221], 0
	v_mfma_f32_16x16x128_f8f6f4 v[62:65], v[18:25], v[222:229], 0
	v_mfma_f32_16x16x128_f8f6f4 v[54:57], v[26:33], v[222:229], 0
	v_mfma_f32_16x16x128_f8f6f4 v[46:49], v[18:25], v[230:237], 0
	v_mfma_f32_16x16x128_f8f6f4 v[38:41], v[26:33], v[230:237], 0
	s_setprio 0
	s_setprio 1
	v_mfma_f32_16x16x128_f8f6f4 v[90:93], v[2:9], v[198:205], 0
	v_mfma_f32_16x16x128_f8f6f4 v[82:85], v[10:17], v[198:205], 0
	v_mfma_f32_16x16x128_f8f6f4 v[74:77], v[2:9], v[214:221], 0
	v_mfma_f32_16x16x128_f8f6f4 v[66:69], v[10:17], v[214:221], 0
	v_mfma_f32_16x16x128_f8f6f4 v[58:61], v[2:9], v[222:229], 0
	v_mfma_f32_16x16x128_f8f6f4 v[50:53], v[10:17], v[222:229], 0
	v_mfma_f32_16x16x128_f8f6f4 v[42:45], v[2:9], v[230:237], 0
	v_mfma_f32_16x16x128_f8f6f4 v[34:37], v[10:17], v[230:237], 0
	s_setprio 0
	s_barrier
	s_branch .Lmidr_0
	.p2align 6

.LBB0_1601:
	s_andn2_b64 vcc, exec, s[12:13]
	s_cbranch_vccnz .Lzs_6
	s_add_i32 s6, s61, 0x80
	s_add_i32 s61, s62, 0x100
	s_mov_b32 s62, 0
	ds_read_b128 v[18:21], v235
	ds_read_b128 v[22:25], v236
	ds_read_b128 v[26:29], v243
	ds_read_b128 v[30:33], v244
	s_waitcnt lgkmcnt(0)
	ds_read_b128 v[2:5], v237
	ds_read_b128 v[6:9], v238
	ds_read_b128 v[10:13], v245
	ds_read_b128 v[14:17], v246
	s_add_i32 s63, s6, 0x80
	s_cmp_eq_u32 s89, s62
	s_cselect_b32 s65, s7, s63
	s_cselect_b32 s64, s5, s61
	s_add_i32 s63, s65, 0x80
	v_mov_b32_e32 v194, v1
	ds_read_b128 v[162:165], v251
	ds_read_b128 v[166:169], v251 offset:1024
	ds_read_b128 v[170:173], v251 offset:2048
	ds_read_b128 v[174:177], v251 offset:3072
	ds_read_b128 v[178:181], v251 offset:4096
	ds_read_b128 v[182:185], v251 offset:5120
	ds_read_b128 v[186:189], v251 offset:6144
	ds_read_b128 v[190:193], v251 offset:7168
	s_add_i32 s66, s6, s86
	v_add_u32_e32 v194, s66, v194
	s_add_i32 m0, s70, 0xc000
	s_add_i32 s66, s6, s93
	global_load_lds_dwordx4 v194, s[8:9]
	v_mov_b32_e32 v194, v1
	s_add_i32 m0, s70, 0xe000
	v_add_u32_e32 v194, s66, v194
	global_load_lds_dwordx4 v194, s[8:9]
	s_waitcnt vmcnt(8)
	s_waitcnt lgkmcnt(0)
	s_barrier
	s_setprio 1
	s_waitcnt lgkmcnt(0)
	v_mfma_f32_16x16x128_f8f6f4 v[158:161], v[18:25], v[162:169], 0
	v_mfma_f32_16x16x128_f8f6f4 v[154:157], v[26:33], v[162:169], 0
	v_mfma_f32_16x16x128_f8f6f4 v[142:145], v[18:25], v[170:177], 0
	v_mfma_f32_16x16x128_f8f6f4 v[138:141], v[26:33], v[170:177], 0
	v_mfma_f32_16x16x128_f8f6f4 v[126:129], v[18:25], v[178:185], 0
	v_mfma_f32_16x16x128_f8f6f4 v[122:125], v[26:33], v[178:185], 0
	v_mfma_f32_16x16x128_f8f6f4 v[110:113], v[18:25], v[186:193], 0
	v_mfma_f32_16x16x128_f8f6f4 v[106:109], v[26:33], v[186:193], 0
	s_setprio 0
	s_setprio 1
	v_mfma_f32_16x16x128_f8f6f4 v[150:153], v[2:9], v[162:169], 0
	v_mfma_f32_16x16x128_f8f6f4 v[146:149], v[10:17], v[162:169], 0
	v_mfma_f32_16x16x128_f8f6f4 v[134:137], v[2:9], v[170:177], 0
	v_mfma_f32_16x16x128_f8f6f4 v[130:133], v[10:17], v[170:177], 0
	v_mfma_f32_16x16x128_f8f6f4 v[118:121], v[2:9], v[178:185], 0
	v_mfma_f32_16x16x128_f8f6f4 v[114:117], v[10:17], v[178:185], 0
	v_mfma_f32_16x16x128_f8f6f4 v[102:105], v[2:9], v[186:193], 0
	v_mfma_f32_16x16x128_f8f6f4 v[98:101], v[10:17], v[186:193], 0
	s_setprio 0
	s_barrier
	v_mov_b32_e32 v194, v211
	ds_read_b128 v[162:165], v251 offset:16384
	ds_read_b128 v[166:169], v251 offset:17408
	ds_read_b128 v[170:173], v251 offset:18432
	ds_read_b128 v[174:177], v251 offset:19456
	ds_read_b128 v[178:181], v251 offset:20480
	ds_read_b128 v[182:185], v251 offset:21504
	ds_read_b128 v[186:189], v251 offset:22528
	ds_read_b128 v[190:193], v251 offset:23552
	s_mov_b32 m0, s71
	v_add_u32_e32 v194, s64, v194
	global_load_lds_dwordx4 v194, s[20:21]
	v_mov_b32_e32 v194, v211
	s_add_i32 s66, s64, s35
	v_add_u32_e32 v194, s66, v194
	s_mov_b32 m0, s72
	s_add_i32 s66, s66, s35
	global_load_lds_dwordx4 v194, s[20:21]
	v_mov_b32_e32 v194, v211
	s_mov_b32 m0, s73
	v_add_u32_e32 v194, s66, v194
	global_load_lds_dwordx4 v194, s[20:21]
	v_mov_b32_e32 v194, v211
	s_add_i32 s66, s66, s35
	v_add_u32_e32 v194, s66, v194
	s_mov_b32 m0, s76
	s_nop 0
	global_load_lds_dwordx4 v194, s[20:21]
	v_mov_b32_e32 v194, v1
	s_mov_b32 m0, s70
	v_add_u32_e32 v194, s65, v194
	global_load_lds_dwordx4 v194, s[8:9]
	v_mov_b32_e32 v194, v1
	s_add_i32 s65, s65, s23
	v_add_u32_e32 v194, s65, v194
	s_mov_b32 m0, s77
	s_nop 0
	global_load_lds_dwordx4 v194, s[8:9]
	s_waitcnt vmcnt(8)
	s_waitcnt lgkmcnt(0)
	s_barrier
	s_setprio 1
	s_waitcnt lgkmcnt(0)
	v_mfma_f32_16x16x128_f8f6f4 v[94:97], v[18:25], v[162:169], 0
	v_mfma_f32_16x16x128_f8f6f4 v[90:93], v[26:33], v[162:169], 0
	v_mfma_f32_16x16x128_f8f6f4 v[78:81], v[18:25], v[170:177], 0
	v_mfma_f32_16x16x128_f8f6f4 v[74:77], v[26:33], v[170:177], 0
	v_mfma_f32_16x16x128_f8f6f4 v[62:65], v[18:25], v[178:185], 0
	v_mfma_f32_16x16x128_f8f6f4 v[58:61], v[26:33], v[178:185], 0
	v_mfma_f32_16x16x128_f8f6f4 v[46:49], v[18:25], v[186:193], 0
	v_mfma_f32_16x16x128_f8f6f4 v[42:45], v[26:33], v[186:193], 0
	s_setprio 0
	s_setprio 1
	v_mfma_f32_16x16x128_f8f6f4 v[86:89], v[2:9], v[162:169], 0
	v_mfma_f32_16x16x128_f8f6f4 v[82:85], v[10:17], v[162:169], 0
	v_mfma_f32_16x16x128_f8f6f4 v[70:73], v[2:9], v[170:177], 0
	v_mfma_f32_16x16x128_f8f6f4 v[66:69], v[10:17], v[170:177], 0
	v_mfma_f32_16x16x128_f8f6f4 v[54:57], v[2:9], v[178:185], 0
	v_mfma_f32_16x16x128_f8f6f4 v[50:53], v[10:17], v[178:185], 0
	v_mfma_f32_16x16x128_f8f6f4 v[38:41], v[2:9], v[186:193], 0
	v_mfma_f32_16x16x128_f8f6f4 v[34:37], v[10:17], v[186:193], 0
	s_setprio 0
	s_barrier
	s_branch .Lmid_5
	.p2align 6

.Lphr_1:
	ds_read_b128 v[132:135], v170
	ds_read_b128 v[136:139], v171
	ds_read_b128 v[140:143], v166
	ds_read_b128 v[154:157], v167
	ds_read_b128 v[188:191], v172
	ds_read_b128 v[192:195], v173
	ds_read_b128 v[196:199], v174
	ds_read_b128 v[200:203], v175
	s_add_i32 s75, s94, 0x80
	s_and_b64 s[50:51], s[50:51], exec
	s_cselect_b32 s50, s75, s49
	s_cselect_b32 s75, s95, s93
	s_add_i32 s51, s75, 0x80
	v_add_u32_e32 v144, s94, v183
	s_add_i32 m0, s52, 0xc000
	ds_read_b128 v[204:207], v184
	ds_read_b128 v[214:217], v184 offset:1024
	ds_read_b128 v[218:221], v184 offset:2048
	ds_read_b128 v[222:225], v184 offset:3072
	ds_read_b128 v[226:229], v184 offset:4096
	ds_read_b128 v[230:233], v184 offset:5120
	ds_read_b128 v[234:237], v184 offset:6144
	ds_read_b128 v[238:241], v184 offset:7168
	global_load_lds_dwordx4 v144, s[8:9]
	v_add_u32_e32 v144, s94, v182
	s_add_i32 m0, s52, 0xe000
	s_nop 0
	global_load_lds_dwordx4 v144, s[8:9]
	s_waitcnt vmcnt(8)
	s_waitcnt lgkmcnt(0)
	s_barrier
	s_setprio 1
	s_waitcnt lgkmcnt(0)
	v_mfma_f32_16x16x32_bf16 v[126:129], v[140:143], v[204:207], 0
	v_mfma_f32_16x16x32_bf16 v[122:125], v[136:139], v[204:207], 0
	v_mfma_f32_16x16x32_bf16 v[110:113], v[140:143], v[218:221], 0
	v_mfma_f32_16x16x32_bf16 v[106:109], v[136:139], v[218:221], 0
	v_mfma_f32_16x16x32_bf16 v[94:97], v[140:143], v[226:229], 0
	v_mfma_f32_16x16x32_bf16 v[90:93], v[136:139], v[226:229], 0
	v_mfma_f32_16x16x32_bf16 v[78:81], v[140:143], v[234:237], 0
	v_mfma_f32_16x16x32_bf16 v[74:77], v[136:139], v[234:237], 0
	v_mfma_f32_16x16x32_bf16 v[126:129], v[132:135], v[214:217], v[126:129]
	v_mfma_f32_16x16x32_bf16 v[122:125], v[188:191], v[214:217], v[122:125]
	v_mfma_f32_16x16x32_bf16 v[110:113], v[132:135], v[222:225], v[110:113]
	v_mfma_f32_16x16x32_bf16 v[106:109], v[188:191], v[222:225], v[106:109]
	v_mfma_f32_16x16x32_bf16 v[94:97], v[132:135], v[230:233], v[94:97]
	v_mfma_f32_16x16x32_bf16 v[90:93], v[188:191], v[230:233], v[90:93]
	v_mfma_f32_16x16x32_bf16 v[78:81], v[132:135], v[238:241], v[78:81]
	v_mfma_f32_16x16x32_bf16 v[74:77], v[188:191], v[238:241], v[74:77]
	s_setprio 0
	s_setprio 1
	v_mfma_f32_16x16x32_bf16 v[118:121], v[154:157], v[204:207], 0
	v_mfma_f32_16x16x32_bf16 v[114:117], v[196:199], v[204:207], 0
	v_mfma_f32_16x16x32_bf16 v[102:105], v[154:157], v[218:221], 0
	v_mfma_f32_16x16x32_bf16 v[98:101], v[196:199], v[218:221], 0
	v_mfma_f32_16x16x32_bf16 v[86:89], v[154:157], v[226:229], 0
	v_mfma_f32_16x16x32_bf16 v[82:85], v[196:199], v[226:229], 0
	v_mfma_f32_16x16x32_bf16 v[70:73], v[154:157], v[234:237], 0
	v_mfma_f32_16x16x32_bf16 v[66:69], v[196:199], v[234:237], 0
	v_mfma_f32_16x16x32_bf16 v[118:121], v[192:195], v[214:217], v[118:121]
	v_mfma_f32_16x16x32_bf16 v[114:117], v[200:203], v[214:217], v[114:117]
	v_mfma_f32_16x16x32_bf16 v[102:105], v[192:195], v[222:225], v[102:105]
	v_mfma_f32_16x16x32_bf16 v[98:101], v[200:203], v[222:225], v[98:101]
	v_mfma_f32_16x16x32_bf16 v[86:89], v[192:195], v[230:233], v[86:89]
	v_mfma_f32_16x16x32_bf16 v[82:85], v[200:203], v[230:233], v[82:85]
	v_mfma_f32_16x16x32_bf16 v[70:73], v[192:195], v[238:241], v[70:73]
	v_mfma_f32_16x16x32_bf16 v[66:69], v[200:203], v[238:241], v[66:69]
	s_setprio 0
	s_barrier
	s_mov_b32 m0, s53
	v_add_u32_e32 v144, s75, v160
	ds_read_b128 v[204:207], v184 offset:16384
	ds_read_b128 v[214:217], v184 offset:17408
	ds_read_b128 v[218:221], v184 offset:18432
	ds_read_b128 v[222:225], v184 offset:19456
	ds_read_b128 v[226:229], v184 offset:20480
	ds_read_b128 v[230:233], v184 offset:21504
	ds_read_b128 v[234:237], v184 offset:22528
	ds_read_b128 v[238:241], v184 offset:23552
	global_load_lds_dwordx4 v144, s[20:21]
	v_add_u32_e32 v144, s45, v144
	s_mov_b32 m0, s54
	s_nop 0
	global_load_lds_dwordx4 v144, s[20:21]
	v_add_u32_e32 v144, s75, v161
	s_mov_b32 m0, s55
	s_nop 0
	global_load_lds_dwordx4 v144, s[20:21]
	v_add_u32_e32 v144, s45, v144
	s_mov_b32 m0, s56
	s_nop 0
	global_load_lds_dwordx4 v144, s[20:21]
	v_add_u32_e32 v144, s50, v1
	s_mov_b32 m0, s52
	s_nop 0
	global_load_lds_dwordx4 v144, s[8:9]
	v_add_u32_e32 v144, s44, v144
	s_mov_b32 m0, s57
	s_nop 0
	global_load_lds_dwordx4 v144, s[8:9]
	s_waitcnt vmcnt(8)
	s_waitcnt lgkmcnt(0)
	s_barrier
	s_setprio 1
	s_waitcnt lgkmcnt(0)
	v_mfma_f32_16x16x32_bf16 v[62:65], v[140:143], v[204:207], 0
	v_mfma_f32_16x16x32_bf16 v[58:61], v[136:139], v[204:207], 0
	v_mfma_f32_16x16x32_bf16 v[46:49], v[140:143], v[218:221], 0
	v_mfma_f32_16x16x32_bf16 v[42:45], v[136:139], v[218:221], 0
	v_mfma_f32_16x16x32_bf16 v[30:33], v[140:143], v[226:229], 0
	v_mfma_f32_16x16x32_bf16 v[26:29], v[136:139], v[226:229], 0
	v_mfma_f32_16x16x32_bf16 v[14:17], v[140:143], v[234:237], 0
	v_mfma_f32_16x16x32_bf16 v[10:13], v[136:139], v[234:237], 0
	v_mfma_f32_16x16x32_bf16 v[62:65], v[132:135], v[214:217], v[62:65]
	v_mfma_f32_16x16x32_bf16 v[58:61], v[188:191], v[214:217], v[58:61]
	v_mfma_f32_16x16x32_bf16 v[46:49], v[132:135], v[222:225], v[46:49]
	v_mfma_f32_16x16x32_bf16 v[42:45], v[188:191], v[222:225], v[42:45]
	v_mfma_f32_16x16x32_bf16 v[30:33], v[132:135], v[230:233], v[30:33]
	v_mfma_f32_16x16x32_bf16 v[26:29], v[188:191], v[230:233], v[26:29]
	v_mfma_f32_16x16x32_bf16 v[14:17], v[132:135], v[238:241], v[14:17]
	v_mfma_f32_16x16x32_bf16 v[10:13], v[188:191], v[238:241], v[10:13]
	s_setprio 0
	s_setprio 1
	v_mfma_f32_16x16x32_bf16 v[54:57], v[154:157], v[204:207], 0
	v_mfma_f32_16x16x32_bf16 v[50:53], v[196:199], v[204:207], 0
	v_mfma_f32_16x16x32_bf16 v[38:41], v[154:157], v[218:221], 0
	v_mfma_f32_16x16x32_bf16 v[34:37], v[196:199], v[218:221], 0
	v_mfma_f32_16x16x32_bf16 v[22:25], v[154:157], v[226:229], 0
	v_mfma_f32_16x16x32_bf16 v[18:21], v[196:199], v[226:229], 0
	v_mfma_f32_16x16x32_bf16 v[6:9], v[154:157], v[234:237], 0
	v_mfma_f32_16x16x32_bf16 v[2:5], v[196:199], v[234:237], 0
	v_mfma_f32_16x16x32_bf16 v[54:57], v[192:195], v[214:217], v[54:57]
	v_mfma_f32_16x16x32_bf16 v[50:53], v[200:203], v[214:217], v[50:53]
	v_mfma_f32_16x16x32_bf16 v[38:41], v[192:195], v[222:225], v[38:41]
	v_mfma_f32_16x16x32_bf16 v[34:37], v[200:203], v[222:225], v[34:37]
	v_mfma_f32_16x16x32_bf16 v[22:25], v[192:195], v[230:233], v[22:25]
	v_mfma_f32_16x16x32_bf16 v[18:21], v[200:203], v[230:233], v[18:21]
	v_mfma_f32_16x16x32_bf16 v[6:9], v[192:195], v[238:241], v[6:9]
	v_mfma_f32_16x16x32_bf16 v[2:5], v[200:203], v[238:241], v[2:5]
	s_setprio 0
	s_barrier
	s_branch .Lmidr_1
	.p2align 6

.LBB0_2045:
	s_andn2_b64 vcc, exec, s[16:17]
	s_cbranch_vccnz .Lzs_8
	s_add_i32 s30, s48, 0x100
	s_mov_b32 s48, 0
	ds_read_b128 v[138:141], v156
	ds_read_b128 v[142:145], v157
	ds_read_b128 v[168:171], v152
	ds_read_b128 v[172:175], v153
	ds_read_b128 v[176:179], v158
	ds_read_b128 v[180:183], v159
	ds_read_b128 v[184:187], v160
	ds_read_b128 v[188:191], v161
	s_add_i32 s49, s48, 2
	s_add_i32 s50, s73, s46
	s_cmp_eq_u32 s71, s48
	s_cselect_b32 s48, s47, s50
	s_cselect_b32 s51, s31, s30
	v_add_u32_e32 v133, s46, v132
	s_add_i32 m0, s52, 0xc000
	ds_read_b128 v[192:195], v131
	ds_read_b128 v[196:199], v131 offset:1024
	ds_read_b128 v[200:203], v131 offset:2048
	ds_read_b128 v[204:207], v131 offset:3072
	ds_read_b128 v[214:217], v131 offset:4096
	ds_read_b128 v[218:221], v131 offset:5120
	ds_read_b128 v[222:225], v131 offset:6144
	ds_read_b128 v[226:229], v131 offset:7168
	global_load_lds_dwordx4 v133, s[6:7]
	v_add_u32_e32 v133, s46, v130
	s_add_i32 m0, s52, 0xe000
	s_nop 0
	global_load_lds_dwordx4 v133, s[6:7]
	s_waitcnt vmcnt(8)
	s_waitcnt lgkmcnt(0)
	s_barrier
	s_setprio 1
	s_waitcnt lgkmcnt(0)
	v_mfma_f32_16x16x32_bf16 v[122:125], v[168:171], v[192:195], 0
	v_mfma_f32_16x16x32_bf16 v[126:129], v[142:145], v[192:195], 0
	v_mfma_f32_16x16x32_bf16 v[110:113], v[168:171], v[200:203], 0
	v_mfma_f32_16x16x32_bf16 v[106:109], v[142:145], v[200:203], 0
	v_mfma_f32_16x16x32_bf16 v[94:97], v[168:171], v[214:217], 0
	v_mfma_f32_16x16x32_bf16 v[90:93], v[142:145], v[214:217], 0
	v_mfma_f32_16x16x32_bf16 v[78:81], v[168:171], v[222:225], 0
	v_mfma_f32_16x16x32_bf16 v[74:77], v[142:145], v[222:225], 0
	v_mfma_f32_16x16x32_bf16 v[122:125], v[138:141], v[196:199], v[122:125]
	v_mfma_f32_16x16x32_bf16 v[126:129], v[176:179], v[196:199], v[126:129]
	v_mfma_f32_16x16x32_bf16 v[110:113], v[138:141], v[204:207], v[110:113]
	v_mfma_f32_16x16x32_bf16 v[106:109], v[176:179], v[204:207], v[106:109]
	v_mfma_f32_16x16x32_bf16 v[94:97], v[138:141], v[218:221], v[94:97]
	v_mfma_f32_16x16x32_bf16 v[90:93], v[176:179], v[218:221], v[90:93]
	v_mfma_f32_16x16x32_bf16 v[78:81], v[138:141], v[226:229], v[78:81]
	v_mfma_f32_16x16x32_bf16 v[74:77], v[176:179], v[226:229], v[74:77]
	s_setprio 0
	s_setprio 1
	v_mfma_f32_16x16x32_bf16 v[118:121], v[172:175], v[192:195], 0
	v_mfma_f32_16x16x32_bf16 v[114:117], v[184:187], v[192:195], 0
	v_mfma_f32_16x16x32_bf16 v[102:105], v[172:175], v[200:203], 0
	v_mfma_f32_16x16x32_bf16 v[98:101], v[184:187], v[200:203], 0
	v_mfma_f32_16x16x32_bf16 v[86:89], v[172:175], v[214:217], 0
	v_mfma_f32_16x16x32_bf16 v[82:85], v[184:187], v[214:217], 0
	v_mfma_f32_16x16x32_bf16 v[70:73], v[172:175], v[222:225], 0
	v_mfma_f32_16x16x32_bf16 v[66:69], v[184:187], v[222:225], 0
	v_mfma_f32_16x16x32_bf16 v[118:121], v[180:183], v[196:199], v[118:121]
	v_mfma_f32_16x16x32_bf16 v[114:117], v[188:191], v[196:199], v[114:117]
	v_mfma_f32_16x16x32_bf16 v[102:105], v[180:183], v[204:207], v[102:105]
	v_mfma_f32_16x16x32_bf16 v[98:101], v[188:191], v[204:207], v[98:101]
	v_mfma_f32_16x16x32_bf16 v[86:89], v[180:183], v[218:221], v[86:89]
	v_mfma_f32_16x16x32_bf16 v[82:85], v[188:191], v[218:221], v[82:85]
	v_mfma_f32_16x16x32_bf16 v[70:73], v[180:183], v[226:229], v[70:73]
	v_mfma_f32_16x16x32_bf16 v[66:69], v[188:191], v[226:229], v[66:69]
	s_setprio 0
	s_barrier
	s_mov_b32 m0, s53
	v_add_u32_e32 v133, s51, v146
	ds_read_b128 v[192:195], v131 offset:16384
	ds_read_b128 v[196:199], v131 offset:17408
	ds_read_b128 v[200:203], v131 offset:18432
	ds_read_b128 v[204:207], v131 offset:19456
	ds_read_b128 v[214:217], v131 offset:20480
	ds_read_b128 v[218:221], v131 offset:21504
	ds_read_b128 v[222:225], v131 offset:22528
	ds_read_b128 v[226:229], v131 offset:23552
	global_load_lds_dwordx4 v133, s[8:9]
	v_add_u32_e32 v133, s45, v133
	s_mov_b32 m0, s54
	s_nop 0
	global_load_lds_dwordx4 v133, s[8:9]
	v_add_u32_e32 v133, s51, v147
	s_mov_b32 m0, s55
	s_nop 0
	global_load_lds_dwordx4 v133, s[8:9]
	v_add_u32_e32 v133, s45, v133
	s_mov_b32 m0, s56
	s_nop 0
	global_load_lds_dwordx4 v133, s[8:9]
	v_add_u32_e32 v133, s48, v1
	s_mov_b32 m0, s52
	s_nop 0
	global_load_lds_dwordx4 v133, s[6:7]
	v_add_u32_e32 v133, s44, v133
	s_mov_b32 m0, s57
	s_nop 0
	global_load_lds_dwordx4 v133, s[6:7]
	s_waitcnt vmcnt(8)
	s_waitcnt lgkmcnt(0)
	s_barrier
	s_setprio 1
	s_waitcnt lgkmcnt(0)
	v_mfma_f32_16x16x32_bf16 v[62:65], v[168:171], v[192:195], 0
	v_mfma_f32_16x16x32_bf16 v[58:61], v[142:145], v[192:195], 0
	v_mfma_f32_16x16x32_bf16 v[46:49], v[168:171], v[200:203], 0
	v_mfma_f32_16x16x32_bf16 v[42:45], v[142:145], v[200:203], 0
	v_mfma_f32_16x16x32_bf16 v[30:33], v[168:171], v[214:217], 0
	v_mfma_f32_16x16x32_bf16 v[26:29], v[142:145], v[214:217], 0
	v_mfma_f32_16x16x32_bf16 v[14:17], v[168:171], v[222:225], 0
	v_mfma_f32_16x16x32_bf16 v[10:13], v[142:145], v[222:225], 0
	v_mfma_f32_16x16x32_bf16 v[62:65], v[138:141], v[196:199], v[62:65]
	v_mfma_f32_16x16x32_bf16 v[58:61], v[176:179], v[196:199], v[58:61]
	v_mfma_f32_16x16x32_bf16 v[46:49], v[138:141], v[204:207], v[46:49]
	v_mfma_f32_16x16x32_bf16 v[42:45], v[176:179], v[204:207], v[42:45]
	v_mfma_f32_16x16x32_bf16 v[30:33], v[138:141], v[218:221], v[30:33]
	v_mfma_f32_16x16x32_bf16 v[26:29], v[176:179], v[218:221], v[26:29]
	v_mfma_f32_16x16x32_bf16 v[14:17], v[138:141], v[226:229], v[14:17]
	v_mfma_f32_16x16x32_bf16 v[10:13], v[176:179], v[226:229], v[10:13]
	s_setprio 0
	s_setprio 1
	v_mfma_f32_16x16x32_bf16 v[54:57], v[172:175], v[192:195], 0
	v_mfma_f32_16x16x32_bf16 v[50:53], v[184:187], v[192:195], 0
	v_mfma_f32_16x16x32_bf16 v[38:41], v[172:175], v[200:203], 0
	v_mfma_f32_16x16x32_bf16 v[34:37], v[184:187], v[200:203], 0
	v_mfma_f32_16x16x32_bf16 v[22:25], v[172:175], v[214:217], 0
	v_mfma_f32_16x16x32_bf16 v[18:21], v[184:187], v[214:217], 0
	v_mfma_f32_16x16x32_bf16 v[6:9], v[172:175], v[222:225], 0
	v_mfma_f32_16x16x32_bf16 v[2:5], v[184:187], v[222:225], 0
	v_mfma_f32_16x16x32_bf16 v[54:57], v[180:183], v[196:199], v[54:57]
	v_mfma_f32_16x16x32_bf16 v[50:53], v[188:191], v[196:199], v[50:53]
	v_mfma_f32_16x16x32_bf16 v[38:41], v[180:183], v[204:207], v[38:41]
	v_mfma_f32_16x16x32_bf16 v[34:37], v[188:191], v[204:207], v[34:37]
	v_mfma_f32_16x16x32_bf16 v[22:25], v[180:183], v[218:221], v[22:25]
	v_mfma_f32_16x16x32_bf16 v[18:21], v[188:191], v[218:221], v[18:21]
	v_mfma_f32_16x16x32_bf16 v[6:9], v[180:183], v[226:229], v[6:9]
	v_mfma_f32_16x16x32_bf16 v[2:5], v[188:191], v[226:229], v[2:5]
	s_setprio 0
	s_barrier
	s_branch .Lmid_6
	.p2align 6

.LBB0_2335:
	s_andn2_b64 vcc, exec, s[14:15]
	s_cbranch_vccnz .Lzs_9
	s_add_i32 s50, s87, 0x80
	s_add_i32 s87, s75, 0x100
	s_mov_b32 s88, 0
	ds_read_b128 v[130:133], v194
	ds_read_b128 v[134:137], v195
	ds_read_b128 v[138:141], v190
	ds_read_b128 v[142:145], v191
	ds_read_b128 v[146:149], v196
	ds_read_b128 v[150:153], v197
	ds_read_b128 v[154:157], v198
	ds_read_b128 v[158:161], v199
	s_add_i32 s75, s50, 0x80
	s_cmp_eq_u32 s70, s88
	s_cselect_b32 s89, s51, s87
	s_cselect_b32 s75, s49, s75
	v_add_u32_e32 v178, s50, v207
	s_add_i32 m0, s53, 0xc000
	ds_read_b128 v[162:165], v208
	ds_read_b128 v[166:169], v208 offset:1024
	ds_read_b128 v[170:173], v208 offset:2048
	ds_read_b128 v[180:183], v208 offset:3072
	ds_read_b128 v[214:217], v208 offset:4096
	ds_read_b128 v[218:221], v208 offset:5120
	ds_read_b128 v[222:225], v208 offset:6144
	ds_read_b128 v[226:229], v208 offset:7168
	global_load_lds_dwordx4 v178, s[4:5]
	v_add_u32_e32 v178, s50, v206
	s_add_i32 m0, s53, 0xe000
	s_nop 0
	global_load_lds_dwordx4 v178, s[4:5]
	s_waitcnt vmcnt(8)
	s_waitcnt lgkmcnt(0)
	s_barrier
	s_setprio 1
	s_waitcnt lgkmcnt(0)
	v_mfma_f32_16x16x32_bf16 v[126:129], v[138:141], v[162:165], 0
	v_mfma_f32_16x16x32_bf16 v[122:125], v[134:137], v[162:165], 0
	v_mfma_f32_16x16x32_bf16 v[110:113], v[138:141], v[170:173], 0
	v_mfma_f32_16x16x32_bf16 v[106:109], v[134:137], v[170:173], 0
	v_mfma_f32_16x16x32_bf16 v[94:97], v[138:141], v[214:217], 0
	v_mfma_f32_16x16x32_bf16 v[90:93], v[134:137], v[214:217], 0
	v_mfma_f32_16x16x32_bf16 v[78:81], v[138:141], v[222:225], 0
	v_mfma_f32_16x16x32_bf16 v[74:77], v[134:137], v[222:225], 0
	v_mfma_f32_16x16x32_bf16 v[126:129], v[130:133], v[166:169], v[126:129]
	v_mfma_f32_16x16x32_bf16 v[122:125], v[146:149], v[166:169], v[122:125]
	v_mfma_f32_16x16x32_bf16 v[110:113], v[130:133], v[180:183], v[110:113]
	v_mfma_f32_16x16x32_bf16 v[106:109], v[146:149], v[180:183], v[106:109]
	v_mfma_f32_16x16x32_bf16 v[94:97], v[130:133], v[218:221], v[94:97]
	v_mfma_f32_16x16x32_bf16 v[90:93], v[146:149], v[218:221], v[90:93]
	v_mfma_f32_16x16x32_bf16 v[78:81], v[130:133], v[226:229], v[78:81]
	v_mfma_f32_16x16x32_bf16 v[74:77], v[146:149], v[226:229], v[74:77]
	s_setprio 0
	s_setprio 1
	v_mfma_f32_16x16x32_bf16 v[118:121], v[142:145], v[162:165], 0
	v_mfma_f32_16x16x32_bf16 v[114:117], v[154:157], v[162:165], 0
	v_mfma_f32_16x16x32_bf16 v[102:105], v[142:145], v[170:173], 0
	v_mfma_f32_16x16x32_bf16 v[98:101], v[154:157], v[170:173], 0
	v_mfma_f32_16x16x32_bf16 v[86:89], v[142:145], v[214:217], 0
	v_mfma_f32_16x16x32_bf16 v[82:85], v[154:157], v[214:217], 0
	v_mfma_f32_16x16x32_bf16 v[70:73], v[142:145], v[222:225], 0
	v_mfma_f32_16x16x32_bf16 v[66:69], v[154:157], v[222:225], 0
	v_mfma_f32_16x16x32_bf16 v[118:121], v[150:153], v[166:169], v[118:121]
	v_mfma_f32_16x16x32_bf16 v[114:117], v[158:161], v[166:169], v[114:117]
	v_mfma_f32_16x16x32_bf16 v[102:105], v[150:153], v[180:183], v[102:105]
	v_mfma_f32_16x16x32_bf16 v[98:101], v[158:161], v[180:183], v[98:101]
	v_mfma_f32_16x16x32_bf16 v[86:89], v[150:153], v[218:221], v[86:89]
	v_mfma_f32_16x16x32_bf16 v[82:85], v[158:161], v[218:221], v[82:85]
	v_mfma_f32_16x16x32_bf16 v[70:73], v[150:153], v[226:229], v[70:73]
	v_mfma_f32_16x16x32_bf16 v[66:69], v[158:161], v[226:229], v[66:69]
	s_setprio 0
	s_barrier
	s_mov_b32 m0, s54
	v_add_u32_e32 v178, s89, v184
	ds_read_b128 v[162:165], v208 offset:16384
	ds_read_b128 v[166:169], v208 offset:17408
	ds_read_b128 v[170:173], v208 offset:18432
	ds_read_b128 v[180:183], v208 offset:19456
	ds_read_b128 v[214:217], v208 offset:20480
	ds_read_b128 v[218:221], v208 offset:21504
	ds_read_b128 v[222:225], v208 offset:22528
	ds_read_b128 v[226:229], v208 offset:23552
	global_load_lds_dwordx4 v178, s[6:7]
	v_add_u32_e32 v178, s52, v178
	s_mov_b32 m0, s55
	s_nop 0
	global_load_lds_dwordx4 v178, s[6:7]
	v_add_u32_e32 v178, s89, v185
	s_mov_b32 m0, s56
	s_nop 0
	global_load_lds_dwordx4 v178, s[6:7]
	v_add_u32_e32 v178, s52, v178
	s_mov_b32 m0, s57
	s_nop 0
	global_load_lds_dwordx4 v178, s[6:7]
	v_add_u32_e32 v178, s75, v1
	s_mov_b32 m0, s53
	s_nop 0
	global_load_lds_dwordx4 v178, s[4:5]
	v_add_u32_e32 v178, s45, v178
	s_mov_b32 m0, s58
	s_nop 0
	global_load_lds_dwordx4 v178, s[4:5]
	s_waitcnt vmcnt(8)
	s_waitcnt lgkmcnt(0)
	s_barrier
	s_setprio 1
	s_waitcnt lgkmcnt(0)
	v_mfma_f32_16x16x32_bf16 v[62:65], v[138:141], v[162:165], 0
	v_mfma_f32_16x16x32_bf16 v[58:61], v[134:137], v[162:165], 0
	v_mfma_f32_16x16x32_bf16 v[46:49], v[138:141], v[170:173], 0
	v_mfma_f32_16x16x32_bf16 v[42:45], v[134:137], v[170:173], 0
	v_mfma_f32_16x16x32_bf16 v[30:33], v[138:141], v[214:217], 0
	v_mfma_f32_16x16x32_bf16 v[26:29], v[134:137], v[214:217], 0
	v_mfma_f32_16x16x32_bf16 v[14:17], v[138:141], v[222:225], 0
	v_mfma_f32_16x16x32_bf16 v[10:13], v[134:137], v[222:225], 0
	v_mfma_f32_16x16x32_bf16 v[62:65], v[130:133], v[166:169], v[62:65]
	v_mfma_f32_16x16x32_bf16 v[58:61], v[146:149], v[166:169], v[58:61]
	v_mfma_f32_16x16x32_bf16 v[46:49], v[130:133], v[180:183], v[46:49]
	v_mfma_f32_16x16x32_bf16 v[42:45], v[146:149], v[180:183], v[42:45]
	v_mfma_f32_16x16x32_bf16 v[30:33], v[130:133], v[218:221], v[30:33]
	v_mfma_f32_16x16x32_bf16 v[26:29], v[146:149], v[218:221], v[26:29]
	v_mfma_f32_16x16x32_bf16 v[14:17], v[130:133], v[226:229], v[14:17]
	v_mfma_f32_16x16x32_bf16 v[10:13], v[146:149], v[226:229], v[10:13]
	s_setprio 0
	s_setprio 1
	v_mfma_f32_16x16x32_bf16 v[54:57], v[142:145], v[162:165], 0
	v_mfma_f32_16x16x32_bf16 v[50:53], v[154:157], v[162:165], 0
	v_mfma_f32_16x16x32_bf16 v[38:41], v[142:145], v[170:173], 0
	v_mfma_f32_16x16x32_bf16 v[34:37], v[154:157], v[170:173], 0
	v_mfma_f32_16x16x32_bf16 v[22:25], v[142:145], v[214:217], 0
	v_mfma_f32_16x16x32_bf16 v[18:21], v[154:157], v[214:217], 0
	v_mfma_f32_16x16x32_bf16 v[6:9], v[142:145], v[222:225], 0
	v_mfma_f32_16x16x32_bf16 v[2:5], v[154:157], v[222:225], 0
	v_mfma_f32_16x16x32_bf16 v[54:57], v[150:153], v[166:169], v[54:57]
	v_mfma_f32_16x16x32_bf16 v[50:53], v[158:161], v[166:169], v[50:53]
	v_mfma_f32_16x16x32_bf16 v[38:41], v[150:153], v[180:183], v[38:41]
	v_mfma_f32_16x16x32_bf16 v[34:37], v[158:161], v[180:183], v[34:37]
	v_mfma_f32_16x16x32_bf16 v[22:25], v[150:153], v[218:221], v[22:25]
	v_mfma_f32_16x16x32_bf16 v[18:21], v[158:161], v[218:221], v[18:21]
	v_mfma_f32_16x16x32_bf16 v[6:9], v[150:153], v[226:229], v[6:9]
	v_mfma_f32_16x16x32_bf16 v[2:5], v[158:161], v[226:229], v[2:5]
	s_setprio 0
	s_barrier
	s_branch .Lmid_7
	.p2align 6

.LBB0_2519:
	s_andn2_b64 vcc, exec, s[14:15]
	s_cbranch_vccnz .Lzs_10
	s_add_i32 s56, s96, 0x80
	s_add_i32 s57, s74, 0x100
	s_mov_b32 s74, 0
	ds_read_b128 v[90:93], v160
	ds_read_b128 v[94:97], v161
	ds_read_b128 v[142:145], v156
	ds_read_b128 v[146:149], v157
	ds_read_b128 v[176:179], v162
	ds_read_b128 v[180:183], v163
	ds_read_b128 v[184:187], v164
	ds_read_b128 v[188:191], v165
	s_add_i32 s96, s56, 0x80
	s_cmp_eq_u32 s81, s74
	s_cselect_b32 vcc_lo, s55, s57
	s_cselect_b32 s96, s45, s96
	v_add_u32_e32 v175, s56, v173
	s_add_i32 m0, s60, 0xc000
	ds_read_b128 v[192:195], v174
	ds_read_b128 v[196:199], v174 offset:1024
	ds_read_b128 v[200:203], v174 offset:2048
	ds_read_b128 v[204:207], v174 offset:3072
	ds_read_b128 v[214:217], v174 offset:4096
	ds_read_b128 v[218:221], v174 offset:5120
	ds_read_b128 v[222:225], v174 offset:6144
	ds_read_b128 v[226:229], v174 offset:7168
	global_load_lds_dwordx4 v175, s[4:5]
	v_add_u32_e32 v175, s56, v172
	s_add_i32 m0, s60, 0xe000
	s_nop 0
	global_load_lds_dwordx4 v175, s[4:5]
	s_waitcnt vmcnt(8)
	s_waitcnt lgkmcnt(0)
	s_barrier
	s_setprio 1
	s_waitcnt lgkmcnt(0)
	v_mfma_f32_16x16x32_bf16 v[134:137], v[142:145], v[192:195], 0
	v_mfma_f32_16x16x32_bf16 v[130:133], v[94:97], v[192:195], 0
	v_mfma_f32_16x16x32_bf16 v[126:129], v[142:145], v[200:203], 0
	v_mfma_f32_16x16x32_bf16 v[122:125], v[94:97], v[200:203], 0
	v_mfma_f32_16x16x32_bf16 v[118:121], v[142:145], v[214:217], 0
	v_mfma_f32_16x16x32_bf16 v[114:117], v[94:97], v[214:217], 0
	v_mfma_f32_16x16x32_bf16 v[110:113], v[142:145], v[222:225], 0
	v_mfma_f32_16x16x32_bf16 v[106:109], v[94:97], v[222:225], 0
	v_mfma_f32_16x16x32_bf16 v[134:137], v[90:93], v[196:199], v[134:137]
	v_mfma_f32_16x16x32_bf16 v[130:133], v[176:179], v[196:199], v[130:133]
	v_mfma_f32_16x16x32_bf16 v[126:129], v[90:93], v[204:207], v[126:129]
	v_mfma_f32_16x16x32_bf16 v[122:125], v[176:179], v[204:207], v[122:125]
	v_mfma_f32_16x16x32_bf16 v[118:121], v[90:93], v[218:221], v[118:121]
	v_mfma_f32_16x16x32_bf16 v[114:117], v[176:179], v[218:221], v[114:117]
	v_mfma_f32_16x16x32_bf16 v[110:113], v[90:93], v[226:229], v[110:113]
	v_mfma_f32_16x16x32_bf16 v[106:109], v[176:179], v[226:229], v[106:109]
	s_setprio 0
	s_setprio 1
	v_mfma_f32_16x16x32_bf16 v[62:65], v[146:149], v[192:195], 0
	v_mfma_f32_16x16x32_bf16 v[58:61], v[184:187], v[192:195], 0
	v_mfma_f32_16x16x32_bf16 v[54:57], v[146:149], v[200:203], 0
	v_mfma_f32_16x16x32_bf16 v[50:53], v[184:187], v[200:203], 0
	v_mfma_f32_16x16x32_bf16 v[46:49], v[146:149], v[214:217], 0
	v_mfma_f32_16x16x32_bf16 v[42:45], v[184:187], v[214:217], 0
	v_mfma_f32_16x16x32_bf16 v[38:41], v[146:149], v[222:225], 0
	v_mfma_f32_16x16x32_bf16 v[34:37], v[184:187], v[222:225], 0
	v_mfma_f32_16x16x32_bf16 v[62:65], v[180:183], v[196:199], v[62:65]
	v_mfma_f32_16x16x32_bf16 v[58:61], v[188:191], v[196:199], v[58:61]
	v_mfma_f32_16x16x32_bf16 v[54:57], v[180:183], v[204:207], v[54:57]
	v_mfma_f32_16x16x32_bf16 v[50:53], v[188:191], v[204:207], v[50:53]
	v_mfma_f32_16x16x32_bf16 v[46:49], v[180:183], v[218:221], v[46:49]
	v_mfma_f32_16x16x32_bf16 v[42:45], v[188:191], v[218:221], v[42:45]
	v_mfma_f32_16x16x32_bf16 v[38:41], v[180:183], v[226:229], v[38:41]
	v_mfma_f32_16x16x32_bf16 v[34:37], v[188:191], v[226:229], v[34:37]
	s_setprio 0
	s_barrier
	s_mov_b32 m0, s61
	v_add_u32_e32 v175, vcc_lo, v150
	ds_read_b128 v[192:195], v174 offset:16384
	ds_read_b128 v[196:199], v174 offset:17408
	ds_read_b128 v[200:203], v174 offset:18432
	ds_read_b128 v[204:207], v174 offset:19456
	ds_read_b128 v[214:217], v174 offset:20480
	ds_read_b128 v[218:221], v174 offset:21504
	ds_read_b128 v[222:225], v174 offset:22528
	ds_read_b128 v[226:229], v174 offset:23552
	global_load_lds_dwordx4 v175, s[6:7]
	v_add_u32_e32 v175, s59, v175
	s_mov_b32 m0, s62
	s_nop 0
	global_load_lds_dwordx4 v175, s[6:7]
	v_add_u32_e32 v175, vcc_lo, v151
	s_mov_b32 m0, s63
	s_nop 0
	global_load_lds_dwordx4 v175, s[6:7]
	v_add_u32_e32 v175, s59, v175
	s_mov_b32 m0, s64
	s_nop 0
	global_load_lds_dwordx4 v175, s[6:7]
	v_add_u32_e32 v175, s96, v1
	s_mov_b32 m0, s60
	s_nop 0
	global_load_lds_dwordx4 v175, s[4:5]
	v_add_u32_e32 v175, s58, v175
	s_mov_b32 m0, s65
	s_nop 0
	global_load_lds_dwordx4 v175, s[4:5]
	s_waitcnt vmcnt(8)
	s_waitcnt lgkmcnt(0)
	s_barrier
	s_setprio 1
	s_waitcnt lgkmcnt(0)
	v_mfma_f32_16x16x32_bf16 v[102:105], v[142:145], v[192:195], 0
	v_mfma_f32_16x16x32_bf16 v[98:101], v[94:97], v[192:195], 0
	v_mfma_f32_16x16x32_bf16 v[86:89], v[142:145], v[200:203], 0
	v_mfma_f32_16x16x32_bf16 v[82:85], v[94:97], v[200:203], 0
	v_mfma_f32_16x16x32_bf16 v[78:81], v[142:145], v[214:217], 0
	v_mfma_f32_16x16x32_bf16 v[74:77], v[94:97], v[214:217], 0
	v_mfma_f32_16x16x32_bf16 v[70:73], v[142:145], v[222:225], 0
	v_mfma_f32_16x16x32_bf16 v[66:69], v[94:97], v[222:225], 0
	v_mfma_f32_16x16x32_bf16 v[102:105], v[90:93], v[196:199], v[102:105]
	v_mfma_f32_16x16x32_bf16 v[98:101], v[176:179], v[196:199], v[98:101]
	v_mfma_f32_16x16x32_bf16 v[86:89], v[90:93], v[204:207], v[86:89]
	v_mfma_f32_16x16x32_bf16 v[82:85], v[176:179], v[204:207], v[82:85]
	v_mfma_f32_16x16x32_bf16 v[78:81], v[90:93], v[218:221], v[78:81]
	v_mfma_f32_16x16x32_bf16 v[74:77], v[176:179], v[218:221], v[74:77]
	v_mfma_f32_16x16x32_bf16 v[70:73], v[90:93], v[226:229], v[70:73]
	v_mfma_f32_16x16x32_bf16 v[66:69], v[176:179], v[226:229], v[66:69]
	s_setprio 0
	s_setprio 1
	v_mfma_f32_16x16x32_bf16 v[30:33], v[146:149], v[192:195], 0
	v_mfma_f32_16x16x32_bf16 v[26:29], v[184:187], v[192:195], 0
	v_mfma_f32_16x16x32_bf16 v[22:25], v[146:149], v[200:203], 0
	v_mfma_f32_16x16x32_bf16 v[18:21], v[184:187], v[200:203], 0
	v_mfma_f32_16x16x32_bf16 v[14:17], v[146:149], v[214:217], 0
	v_mfma_f32_16x16x32_bf16 v[10:13], v[184:187], v[214:217], 0
	v_mfma_f32_16x16x32_bf16 v[6:9], v[146:149], v[222:225], 0
	v_mfma_f32_16x16x32_bf16 v[2:5], v[184:187], v[222:225], 0
	v_mfma_f32_16x16x32_bf16 v[30:33], v[180:183], v[196:199], v[30:33]
	v_mfma_f32_16x16x32_bf16 v[26:29], v[188:191], v[196:199], v[26:29]
	v_mfma_f32_16x16x32_bf16 v[22:25], v[180:183], v[204:207], v[22:25]
	v_mfma_f32_16x16x32_bf16 v[18:21], v[188:191], v[204:207], v[18:21]
	v_mfma_f32_16x16x32_bf16 v[14:17], v[180:183], v[218:221], v[14:17]
	v_mfma_f32_16x16x32_bf16 v[10:13], v[188:191], v[218:221], v[10:13]
	v_mfma_f32_16x16x32_bf16 v[6:9], v[180:183], v[226:229], v[6:9]
	v_mfma_f32_16x16x32_bf16 v[2:5], v[188:191], v[226:229], v[2:5]
	s_setprio 0
	s_barrier
	s_branch .Lmid_8
	.p2align 6

.LBB0_2595:
	s_andn2_b64 vcc, exec, s[12:13]
	s_cbranch_vccnz .Lzs_11
	s_add_i32 s60, s64, 0x80
	s_addk_i32 s63, 0x100
	s_mov_b32 s64, 0
	ds_read_b128 v[130:133], v206
	ds_read_b128 v[134:137], v207
	ds_read_b128 v[138:141], v202
	ds_read_b128 v[142:145], v203
	ds_read_b128 v[146:149], v208
	ds_read_b128 v[150:153], v209
	ds_read_b128 v[154:157], v211
	ds_read_b128 v[158:161], v213
	s_add_i32 s65, s60, 0x80
	s_cmp_eq_u32 s84, s64
	s_cselect_b32 s75, s61, s63
	s_cselect_b32 s65, s5, s65
	v_add_u32_e32 v194, s60, v221
	s_add_i32 m0, s45, 0xc000
	ds_read_b128 v[162:165], v222
	ds_read_b128 v[166:169], v222 offset:1024
	ds_read_b128 v[170:173], v222 offset:2048
	ds_read_b128 v[174:177], v222 offset:3072
	ds_read_b128 v[182:185], v222 offset:4096
	ds_read_b128 v[186:189], v222 offset:5120
	ds_read_b128 v[190:193], v222 offset:6144
	ds_read_b128 v[224:227], v222 offset:7168
	global_load_lds_dwordx4 v194, s[6:7]
	v_add_u32_e32 v194, s60, v220
	s_add_i32 m0, s45, 0xe000
	s_nop 0
	global_load_lds_dwordx4 v194, s[6:7]
	s_waitcnt vmcnt(8)
	s_waitcnt lgkmcnt(0)
	s_barrier
	s_setprio 1
	s_waitcnt lgkmcnt(0)
	v_mfma_f32_16x16x32_bf16 v[126:129], v[138:141], v[162:165], 0
	v_mfma_f32_16x16x32_bf16 v[122:125], v[134:137], v[162:165], 0
	v_mfma_f32_16x16x32_bf16 v[110:113], v[138:141], v[170:173], 0
	v_mfma_f32_16x16x32_bf16 v[106:109], v[134:137], v[170:173], 0
	v_mfma_f32_16x16x32_bf16 v[94:97], v[138:141], v[182:185], 0
	v_mfma_f32_16x16x32_bf16 v[90:93], v[134:137], v[182:185], 0
	v_mfma_f32_16x16x32_bf16 v[78:81], v[138:141], v[190:193], 0
	v_mfma_f32_16x16x32_bf16 v[74:77], v[134:137], v[190:193], 0
	v_mfma_f32_16x16x32_bf16 v[126:129], v[130:133], v[166:169], v[126:129]
	v_mfma_f32_16x16x32_bf16 v[122:125], v[146:149], v[166:169], v[122:125]
	v_mfma_f32_16x16x32_bf16 v[110:113], v[130:133], v[174:177], v[110:113]
	v_mfma_f32_16x16x32_bf16 v[106:109], v[146:149], v[174:177], v[106:109]
	v_mfma_f32_16x16x32_bf16 v[94:97], v[130:133], v[186:189], v[94:97]
	v_mfma_f32_16x16x32_bf16 v[90:93], v[146:149], v[186:189], v[90:93]
	v_mfma_f32_16x16x32_bf16 v[78:81], v[130:133], v[224:227], v[78:81]
	v_mfma_f32_16x16x32_bf16 v[74:77], v[146:149], v[224:227], v[74:77]
	s_setprio 0
	s_setprio 1
	v_mfma_f32_16x16x32_bf16 v[118:121], v[142:145], v[162:165], 0
	v_mfma_f32_16x16x32_bf16 v[114:117], v[154:157], v[162:165], 0
	v_mfma_f32_16x16x32_bf16 v[102:105], v[142:145], v[170:173], 0
	v_mfma_f32_16x16x32_bf16 v[98:101], v[154:157], v[170:173], 0
	v_mfma_f32_16x16x32_bf16 v[86:89], v[142:145], v[182:185], 0
	v_mfma_f32_16x16x32_bf16 v[82:85], v[154:157], v[182:185], 0
	v_mfma_f32_16x16x32_bf16 v[70:73], v[142:145], v[190:193], 0
	v_mfma_f32_16x16x32_bf16 v[66:69], v[154:157], v[190:193], 0
	v_mfma_f32_16x16x32_bf16 v[118:121], v[150:153], v[166:169], v[118:121]
	v_mfma_f32_16x16x32_bf16 v[114:117], v[158:161], v[166:169], v[114:117]
	v_mfma_f32_16x16x32_bf16 v[102:105], v[150:153], v[174:177], v[102:105]
	v_mfma_f32_16x16x32_bf16 v[98:101], v[158:161], v[174:177], v[98:101]
	v_mfma_f32_16x16x32_bf16 v[86:89], v[150:153], v[186:189], v[86:89]
	v_mfma_f32_16x16x32_bf16 v[82:85], v[158:161], v[186:189], v[82:85]
	v_mfma_f32_16x16x32_bf16 v[70:73], v[150:153], v[224:227], v[70:73]
	v_mfma_f32_16x16x32_bf16 v[66:69], v[158:161], v[224:227], v[66:69]
	s_setprio 0
	s_barrier
	s_mov_b32 m0, s66
	v_add_u32_e32 v194, s75, v196
	ds_read_b128 v[162:165], v222 offset:16384
	ds_read_b128 v[166:169], v222 offset:17408
	ds_read_b128 v[170:173], v222 offset:18432
	ds_read_b128 v[174:177], v222 offset:19456
	ds_read_b128 v[182:185], v222 offset:20480
	ds_read_b128 v[186:189], v222 offset:21504
	ds_read_b128 v[190:193], v222 offset:22528
	ds_read_b128 v[224:227], v222 offset:23552
	global_load_lds_dwordx4 v194, s[8:9]
	v_add_u32_e32 v194, s44, v194
	s_mov_b32 m0, s67
	s_nop 0
	global_load_lds_dwordx4 v194, s[8:9]
	v_add_u32_e32 v194, s75, v197
	s_mov_b32 m0, s68
	s_nop 0
	global_load_lds_dwordx4 v194, s[8:9]
	v_add_u32_e32 v194, s44, v194
	s_mov_b32 m0, s69
	s_nop 0
	global_load_lds_dwordx4 v194, s[8:9]
	v_add_u32_e32 v194, s65, v1
	s_mov_b32 m0, s45
	s_nop 0
	global_load_lds_dwordx4 v194, s[6:7]
	v_add_u32_e32 v194, s35, v194
	s_mov_b32 m0, s70
	s_nop 0
	global_load_lds_dwordx4 v194, s[6:7]
	s_waitcnt vmcnt(8)
	s_waitcnt lgkmcnt(0)
	s_barrier
	s_setprio 1
	s_waitcnt lgkmcnt(0)
	v_mfma_f32_16x16x32_bf16 v[62:65], v[138:141], v[162:165], 0
	v_mfma_f32_16x16x32_bf16 v[58:61], v[134:137], v[162:165], 0
	v_mfma_f32_16x16x32_bf16 v[46:49], v[138:141], v[170:173], 0
	v_mfma_f32_16x16x32_bf16 v[42:45], v[134:137], v[170:173], 0
	v_mfma_f32_16x16x32_bf16 v[30:33], v[138:141], v[182:185], 0
	v_mfma_f32_16x16x32_bf16 v[26:29], v[134:137], v[182:185], 0
	v_mfma_f32_16x16x32_bf16 v[14:17], v[138:141], v[190:193], 0
	v_mfma_f32_16x16x32_bf16 v[10:13], v[134:137], v[190:193], 0
	v_mfma_f32_16x16x32_bf16 v[62:65], v[130:133], v[166:169], v[62:65]
	v_mfma_f32_16x16x32_bf16 v[58:61], v[146:149], v[166:169], v[58:61]
	v_mfma_f32_16x16x32_bf16 v[46:49], v[130:133], v[174:177], v[46:49]
	v_mfma_f32_16x16x32_bf16 v[42:45], v[146:149], v[174:177], v[42:45]
	v_mfma_f32_16x16x32_bf16 v[30:33], v[130:133], v[186:189], v[30:33]
	v_mfma_f32_16x16x32_bf16 v[26:29], v[146:149], v[186:189], v[26:29]
	v_mfma_f32_16x16x32_bf16 v[14:17], v[130:133], v[224:227], v[14:17]
	v_mfma_f32_16x16x32_bf16 v[10:13], v[146:149], v[224:227], v[10:13]
	s_setprio 0
	s_setprio 1
	v_mfma_f32_16x16x32_bf16 v[54:57], v[142:145], v[162:165], 0
	v_mfma_f32_16x16x32_bf16 v[50:53], v[154:157], v[162:165], 0
	v_mfma_f32_16x16x32_bf16 v[38:41], v[142:145], v[170:173], 0
	v_mfma_f32_16x16x32_bf16 v[34:37], v[154:157], v[170:173], 0
	v_mfma_f32_16x16x32_bf16 v[22:25], v[142:145], v[182:185], 0
	v_mfma_f32_16x16x32_bf16 v[18:21], v[154:157], v[182:185], 0
	v_mfma_f32_16x16x32_bf16 v[6:9], v[142:145], v[190:193], 0
	v_mfma_f32_16x16x32_bf16 v[2:5], v[154:157], v[190:193], 0
	v_mfma_f32_16x16x32_bf16 v[54:57], v[150:153], v[166:169], v[54:57]
	v_mfma_f32_16x16x32_bf16 v[50:53], v[158:161], v[166:169], v[50:53]
	v_mfma_f32_16x16x32_bf16 v[38:41], v[150:153], v[174:177], v[38:41]
	v_mfma_f32_16x16x32_bf16 v[34:37], v[158:161], v[174:177], v[34:37]
	v_mfma_f32_16x16x32_bf16 v[22:25], v[150:153], v[186:189], v[22:25]
	v_mfma_f32_16x16x32_bf16 v[18:21], v[158:161], v[186:189], v[18:21]
	v_mfma_f32_16x16x32_bf16 v[6:9], v[150:153], v[224:227], v[6:9]
	v_mfma_f32_16x16x32_bf16 v[2:5], v[158:161], v[224:227], v[2:5]
	s_setprio 0
	s_barrier
	s_branch .Lmid_9
	.p2align 6

.LBB0_2935:
	s_andn2_b64 vcc, exec, s[14:15]
	s_cbranch_vccnz .Lzs_12
	s_add_i32 s28, s82, 0x80
	s_add_i32 s82, s83, 0x100
	s_mov_b32 s83, 0
	ds_read_b128 v[18:21], v180
	ds_read_b128 v[22:25], v181
	ds_read_b128 v[26:29], v188
	ds_read_b128 v[30:33], v189
	ds_read_b128 v[2:5], v182
	ds_read_b128 v[6:9], v183
	ds_read_b128 v[10:13], v190
	ds_read_b128 v[14:17], v191
	s_add_i32 s84, s28, 0x80
	s_cmp_eq_u32 s67, s83
	s_cselect_b32 s86, s25, s84
	s_cselect_b32 s87, s29, s82
	s_add_i32 s84, s86, 0x80
	s_add_i32 s85, s87, 0x80
	v_mov_b32_e32 v172, v176
	ds_read_b128 v[164:167], v196
	ds_read_b128 v[168:171], v196 offset:1024
	ds_read_b128 v[198:201], v196 offset:2048
	ds_read_b128 v[202:205], v196 offset:3072
	ds_read_b128 v[214:217], v196 offset:4096
	ds_read_b128 v[218:221], v196 offset:5120
	ds_read_b128 v[222:225], v196 offset:6144
	ds_read_b128 v[226:229], v196 offset:7168
	s_add_i32 s88, s28, s65
	v_add_u32_e32 v172, s88, v172
	s_add_i32 m0, s49, 0xc000
	s_add_i32 s88, s28, s70
	global_load_lds_dwordx4 v172, s[4:5]
	v_mov_b32_e32 v172, v176
	s_add_i32 m0, s49, 0xe000
	v_add_u32_e32 v172, s88, v172
	global_load_lds_dwordx4 v172, s[4:5]
	s_waitcnt vmcnt(8)
	s_waitcnt lgkmcnt(0)
	s_barrier
	s_setprio 1
	s_waitcnt lgkmcnt(0)
	v_mfma_f32_16x16x128_f8f6f4 v[158:161], v[18:25], v[164:171], 0
	v_mfma_f32_16x16x128_f8f6f4 v[154:157], v[26:33], v[164:171], 0
	v_mfma_f32_16x16x128_f8f6f4 v[150:153], v[18:25], v[198:205], 0
	v_mfma_f32_16x16x128_f8f6f4 v[146:149], v[26:33], v[198:205], 0
	v_mfma_f32_16x16x128_f8f6f4 v[138:141], v[18:25], v[214:221], 0
	v_mfma_f32_16x16x128_f8f6f4 v[130:133], v[26:33], v[214:221], 0
	v_mfma_f32_16x16x128_f8f6f4 v[122:125], v[18:25], v[222:229], 0
	v_mfma_f32_16x16x128_f8f6f4 v[114:117], v[26:33], v[222:229], 0
	s_setprio 0
	s_setprio 1
	v_mfma_f32_16x16x128_f8f6f4 v[142:145], v[2:9], v[164:171], 0
	v_mfma_f32_16x16x128_f8f6f4 v[134:137], v[10:17], v[164:171], 0
	v_mfma_f32_16x16x128_f8f6f4 v[126:129], v[2:9], v[198:205], 0
	v_mfma_f32_16x16x128_f8f6f4 v[118:121], v[10:17], v[198:205], 0
	v_mfma_f32_16x16x128_f8f6f4 v[110:113], v[2:9], v[214:221], 0
	v_mfma_f32_16x16x128_f8f6f4 v[106:109], v[10:17], v[214:221], 0
	v_mfma_f32_16x16x128_f8f6f4 v[102:105], v[2:9], v[222:229], 0
	v_mfma_f32_16x16x128_f8f6f4 v[98:101], v[10:17], v[222:229], 0
	s_setprio 0
	s_barrier
	v_mov_b32_e32 v172, v177
	ds_read_b128 v[164:167], v196 offset:16384
	ds_read_b128 v[168:171], v196 offset:17408
	ds_read_b128 v[198:201], v196 offset:18432
	ds_read_b128 v[202:205], v196 offset:19456
	ds_read_b128 v[214:217], v196 offset:20480
	ds_read_b128 v[218:221], v196 offset:21504
	ds_read_b128 v[222:225], v196 offset:22528
	ds_read_b128 v[226:229], v196 offset:23552
	s_mov_b32 m0, s50
	v_add_u32_e32 v172, s87, v172
	global_load_lds_dwordx4 v172, s[6:7]
	v_mov_b32_e32 v172, v177
	s_add_i32 s87, s87, s48
	v_add_u32_e32 v172, s87, v172
	s_mov_b32 m0, s51
	s_add_i32 s87, s87, s48
	global_load_lds_dwordx4 v172, s[6:7]
	v_mov_b32_e32 v172, v177
	s_mov_b32 m0, s52
	v_add_u32_e32 v172, s87, v172
	global_load_lds_dwordx4 v172, s[6:7]
	v_mov_b32_e32 v172, v177
	s_add_i32 s87, s87, s48
	v_add_u32_e32 v172, s87, v172
	s_mov_b32 m0, s53
	s_nop 0
	global_load_lds_dwordx4 v172, s[6:7]
	v_mov_b32_e32 v172, v176
	s_mov_b32 m0, s49
	v_add_u32_e32 v172, s86, v172
	global_load_lds_dwordx4 v172, s[4:5]
	v_mov_b32_e32 v172, v176
	s_add_i32 s86, s86, s47
	v_add_u32_e32 v172, s86, v172
	s_mov_b32 m0, s54
	s_nop 0
	global_load_lds_dwordx4 v172, s[4:5]
	s_waitcnt vmcnt(8)
	s_waitcnt lgkmcnt(0)
	s_barrier
	s_setprio 1
	s_waitcnt lgkmcnt(0)
	v_mfma_f32_16x16x128_f8f6f4 v[94:97], v[18:25], v[164:171], 0
	v_mfma_f32_16x16x128_f8f6f4 v[90:93], v[26:33], v[164:171], 0
	v_mfma_f32_16x16x128_f8f6f4 v[86:89], v[18:25], v[198:205], 0
	v_mfma_f32_16x16x128_f8f6f4 v[82:85], v[26:33], v[198:205], 0
	v_mfma_f32_16x16x128_f8f6f4 v[74:77], v[18:25], v[214:221], 0
	v_mfma_f32_16x16x128_f8f6f4 v[66:69], v[26:33], v[214:221], 0
	v_mfma_f32_16x16x128_f8f6f4 v[58:61], v[18:25], v[222:229], 0
	v_mfma_f32_16x16x128_f8f6f4 v[50:53], v[26:33], v[222:229], 0
	s_setprio 0
	s_setprio 1
	v_mfma_f32_16x16x128_f8f6f4 v[78:81], v[2:9], v[164:171], 0
	v_mfma_f32_16x16x128_f8f6f4 v[70:73], v[10:17], v[164:171], 0
	v_mfma_f32_16x16x128_f8f6f4 v[62:65], v[2:9], v[198:205], 0
	v_mfma_f32_16x16x128_f8f6f4 v[54:57], v[10:17], v[198:205], 0
	v_mfma_f32_16x16x128_f8f6f4 v[46:49], v[2:9], v[214:221], 0
	v_mfma_f32_16x16x128_f8f6f4 v[42:45], v[10:17], v[214:221], 0
	v_mfma_f32_16x16x128_f8f6f4 v[38:41], v[2:9], v[222:229], 0
	v_mfma_f32_16x16x128_f8f6f4 v[34:37], v[10:17], v[222:229], 0
	s_setprio 0
	s_barrier
	s_branch .Lmid_10
	.p2align 6

.LBB0_3005:
	s_andn2_b64 vcc, exec, s[12:13]
	v_mov_b64_e32 v[2:3], 0
	v_mov_b64_e32 v[4:5], 0
	v_mov_b64_e32 v[6:7], 0
	v_mov_b64_e32 v[8:9], 0
	v_mov_b64_e32 v[10:11], 0
	v_mov_b64_e32 v[12:13], 0
	v_mov_b64_e32 v[14:15], 0
	v_mov_b64_e32 v[16:17], 0
	v_mov_b64_e32 v[18:19], 0
	v_mov_b64_e32 v[20:21], 0
	v_mov_b64_e32 v[22:23], 0
	v_mov_b64_e32 v[24:25], 0
	v_mov_b64_e32 v[26:27], 0
	v_mov_b64_e32 v[28:29], 0
	v_mov_b64_e32 v[30:31], 0
	v_mov_b64_e32 v[32:33], 0
	s_cbranch_vccnz .Lzs_13
	s_add_i32 s20, s74, 0x80
	s_add_i32 s74, s75, 0x100
	s_mov_b32 s75, 0
	ds_read_b128 v[18:21], v168
	ds_read_b128 v[22:25], v169
	ds_read_b128 v[26:29], v176
	ds_read_b128 v[30:33], v177
	ds_read_b128 v[2:5], v170
	ds_read_b128 v[6:9], v171
	ds_read_b128 v[10:13], v178
	ds_read_b128 v[14:17], v179
	s_add_i32 s76, s20, 0x80
	s_cmp_eq_u32 s61, s75
	s_cselect_b32 s78, s11, s76
	s_cselect_b32 s77, s21, s74
	s_add_i32 s76, s78, 0x80
	v_mov_b32_e32 v185, v164
	ds_read_b128 v[186:189], v184
	ds_read_b128 v[190:193], v184 offset:1024
	ds_read_b128 v[194:197], v184 offset:2048
	ds_read_b128 v[198:201], v184 offset:3072
	ds_read_b128 v[202:205], v184 offset:4096
	ds_read_b128 v[206:209], v184 offset:5120
	ds_read_b128 v[214:217], v184 offset:6144
	ds_read_b128 v[218:221], v184 offset:7168
	s_add_i32 s79, s20, s59
	v_add_u32_e32 v185, s79, v185
	s_add_i32 m0, s30, 0xc000
	s_add_i32 s79, s20, s66
	global_load_lds_dwordx4 v185, s[4:5]
	v_mov_b32_e32 v185, v164
	s_add_i32 m0, s30, 0xe000
	v_add_u32_e32 v185, s79, v185
	global_load_lds_dwordx4 v185, s[4:5]
	s_waitcnt vmcnt(8)
	s_waitcnt lgkmcnt(0)
	s_barrier
	s_setprio 1
	s_waitcnt lgkmcnt(0)
	v_mfma_f32_16x16x128_f8f6f4 v[158:161], v[18:25], v[186:193], 0
	v_mfma_f32_16x16x128_f8f6f4 v[154:157], v[26:33], v[186:193], 0
	v_mfma_f32_16x16x128_f8f6f4 v[150:153], v[18:25], v[194:201], 0
	v_mfma_f32_16x16x128_f8f6f4 v[146:149], v[26:33], v[194:201], 0
	v_mfma_f32_16x16x128_f8f6f4 v[138:141], v[18:25], v[202:209], 0
	v_mfma_f32_16x16x128_f8f6f4 v[130:133], v[26:33], v[202:209], 0
	v_mfma_f32_16x16x128_f8f6f4 v[122:125], v[18:25], v[214:221], 0
	v_mfma_f32_16x16x128_f8f6f4 v[114:117], v[26:33], v[214:221], 0
	s_setprio 0
	s_setprio 1
	v_mfma_f32_16x16x128_f8f6f4 v[142:145], v[2:9], v[186:193], 0
	v_mfma_f32_16x16x128_f8f6f4 v[134:137], v[10:17], v[186:193], 0
	v_mfma_f32_16x16x128_f8f6f4 v[126:129], v[2:9], v[194:201], 0
	v_mfma_f32_16x16x128_f8f6f4 v[118:121], v[10:17], v[194:201], 0
	v_mfma_f32_16x16x128_f8f6f4 v[110:113], v[2:9], v[202:209], 0
	v_mfma_f32_16x16x128_f8f6f4 v[106:109], v[10:17], v[202:209], 0
	v_mfma_f32_16x16x128_f8f6f4 v[102:105], v[2:9], v[214:221], 0
	v_mfma_f32_16x16x128_f8f6f4 v[98:101], v[10:17], v[214:221], 0
	s_setprio 0
	s_barrier
	v_mov_b32_e32 v185, v165
	ds_read_b128 v[186:189], v184 offset:16384
	ds_read_b128 v[190:193], v184 offset:17408
	ds_read_b128 v[194:197], v184 offset:18432
	ds_read_b128 v[198:201], v184 offset:19456
	ds_read_b128 v[202:205], v184 offset:20480
	ds_read_b128 v[206:209], v184 offset:21504
	ds_read_b128 v[214:217], v184 offset:22528
	ds_read_b128 v[218:221], v184 offset:23552
	s_mov_b32 m0, s31
	v_add_u32_e32 v185, s77, v185
	global_load_lds_dwordx4 v185, s[6:7]
	v_mov_b32_e32 v185, v165
	s_add_i32 s79, s77, s25
	v_add_u32_e32 v185, s79, v185
	s_mov_b32 m0, s35
	s_add_i32 s79, s79, s25
	global_load_lds_dwordx4 v185, s[6:7]
	v_mov_b32_e32 v185, v165
	s_mov_b32 m0, s44
	v_add_u32_e32 v185, s79, v185
	global_load_lds_dwordx4 v185, s[6:7]
	v_mov_b32_e32 v185, v165
	s_add_i32 s79, s79, s25
	v_add_u32_e32 v185, s79, v185
	s_mov_b32 m0, s45
	s_nop 0
	global_load_lds_dwordx4 v185, s[6:7]
	v_mov_b32_e32 v185, v164
	s_mov_b32 m0, s30
	v_add_u32_e32 v185, s78, v185
	global_load_lds_dwordx4 v185, s[4:5]
	v_mov_b32_e32 v185, v164
	s_add_i32 s78, s78, s24
	v_add_u32_e32 v185, s78, v185
	s_mov_b32 m0, s46
	s_nop 0
	global_load_lds_dwordx4 v185, s[4:5]
	s_waitcnt vmcnt(8)
	s_waitcnt lgkmcnt(0)
	s_barrier
	s_setprio 1
	s_waitcnt lgkmcnt(0)
	v_mfma_f32_16x16x128_f8f6f4 v[94:97], v[18:25], v[186:193], 0
	v_mfma_f32_16x16x128_f8f6f4 v[90:93], v[26:33], v[186:193], 0
	v_mfma_f32_16x16x128_f8f6f4 v[86:89], v[18:25], v[194:201], 0
	v_mfma_f32_16x16x128_f8f6f4 v[82:85], v[26:33], v[194:201], 0
	v_mfma_f32_16x16x128_f8f6f4 v[74:77], v[18:25], v[202:209], 0
	v_mfma_f32_16x16x128_f8f6f4 v[66:69], v[26:33], v[202:209], 0
	v_mfma_f32_16x16x128_f8f6f4 v[58:61], v[18:25], v[214:221], 0
	v_mfma_f32_16x16x128_f8f6f4 v[50:53], v[26:33], v[214:221], 0
	s_setprio 0
	s_setprio 1
	v_mfma_f32_16x16x128_f8f6f4 v[78:81], v[2:9], v[186:193], 0
	v_mfma_f32_16x16x128_f8f6f4 v[70:73], v[10:17], v[186:193], 0
	v_mfma_f32_16x16x128_f8f6f4 v[62:65], v[2:9], v[194:201], 0
	v_mfma_f32_16x16x128_f8f6f4 v[54:57], v[10:17], v[194:201], 0
	v_mfma_f32_16x16x128_f8f6f4 v[46:49], v[2:9], v[202:209], 0
	v_mfma_f32_16x16x128_f8f6f4 v[42:45], v[10:17], v[202:209], 0
	v_mfma_f32_16x16x128_f8f6f4 v[38:41], v[2:9], v[214:221], 0
	v_mfma_f32_16x16x128_f8f6f4 v[34:37], v[10:17], v[214:221], 0
	s_setprio 0
	s_barrier
	s_branch .Lmid_11
	.p2align 6
